# speedup vs baseline: 1.0248x; 1.0186x over previous
_Z13attn11_kernelILi4EEvPc:
	s_ashr_i32 s5, s2, 3
	s_load_dwordx2 s[12:13], s[0:1], 0x0
	s_lshr_b32 s4, s5, 29
	s_lshl_b32 s3, s2, 4
	s_add_i32 s6, s5, s4
	s_and_b32 s3, s3, 0x70
	s_ashr_i32 s4, s6, 3
	s_add_i32 s4, s3, s4
	s_and_b32 s3, s6, 0x1fffff8
	s_sub_i32 s3, s5, s3
	v_lshrrev_b32_e32 v1, 6, v0
	s_waitcnt lgkmcnt(0)
	s_add_u32 s14, s12, 0x2500000
	v_lshlrev_b32_e32 v192, 5, v1
	s_addc_u32 s15, s13, 0
	s_ashr_i32 s5, s4, 31
	s_mul_i32 s6, s4, 0x12000
	v_lshl_or_b32 v172, s3, 7, v192
	s_mul_hi_i32 s3, s4, 0x12000
	s_add_u32 s8, s14, s6
	s_addc_u32 s9, s15, s3
	s_add_u32 s16, s12, 0x3700000
	v_lshlrev_b32_e32 v169, 4, v0
	s_addc_u32 s17, s13, 0
	s_add_u32 s10, s16, s6
	v_add_u32_e32 v193, 0, v169
	v_lshrrev_b32_e32 v2, 2, v0
	v_bitop3_b32 v3, v169, 48, v0 bitop3:0x48
	s_addc_u32 s11, s17, s3
	s_mov_b64 s[46:47], s[8:9]
	s_mov_b64 s[48:49], s[10:11]
	s_mov_b64 s[50:51], s[14:15]
	s_mov_b64 s[52:53], s[16:17]
	v_readfirstlane_b32 s3, v193
	v_add_u32_e32 v4, 0x8000, v193
	v_lshl_or_b32 v170, v2, 6, v3
	v_mul_u32_u24_e32 v2, 0x480, v2
	v_mov_b32_e32 v171, 0
	s_mov_b32 m0, s3
	v_readfirstlane_b32 s3, v4
	v_add_u32_e32 v6, 0x2000, v193
	v_or_b32_e32 v2, v2, v3
	v_lshl_add_u64 v[174:175], s[8:9], 0, v[170:171]
	v_mov_b32_e32 v3, v171
	global_load_lds_dwordx4 v170, s[8:9]
	v_mov_b32_e32 v220, v170
	s_mov_b32 m0, s3
	s_mov_b64 s[8:9], 0x1000
	v_readfirstlane_b32 s6, v6
	v_add_u32_e32 v6, 0x4000, v193
	v_lshl_add_u64 v[176:177], s[10:11], 0, v[2:3]
	global_load_lds_dwordx4 v2, s[10:11]
	v_mov_b32_e32 v221, v2
	v_lshl_add_u64 v[4:5], v[174:175], 0, s[8:9]
	s_mov_b32 m0, s6
	s_mov_b64 s[10:11], 0x2000
	v_readfirstlane_b32 s6, v6
	v_add_u32_e32 v6, 0xa000, v193
	global_load_lds_dwordx4 v[4:5], off
	v_lshl_add_u64 v[4:5], v[174:175], 0, s[10:11]
	s_mov_b32 m0, s6
	v_readfirstlane_b32 s6, v6
	s_add_u32 s18, s12, 0x1500000
	global_load_lds_dwordx4 v[4:5], off
	v_lshl_add_u64 v[4:5], v[176:177], 0, 64
	s_mov_b32 m0, s6
	s_addc_u32 s19, s13, 0
	s_lshl_b64 s[20:21], s[4:5], 10
	v_ashrrev_i32_e32 v173, 31, v172
	v_and_b32_e32 v168, 31, v0
	global_load_lds_dwordx4 v[4:5], off
	v_lshl_add_u64 v[4:5], s[20:21], 0, v[172:173]
	v_or_b32_e32 v4, v4, v168
	v_lshlrev_b64 v[4:5], 6, v[4:5]
	v_lshl_add_u64 v[4:5], s[18:19], 0, v[4:5]
	v_and_b32_e32 v6, 32, v0
	v_mov_b32_e32 v7, v171
	v_lshl_add_u64 v[4:5], v[4:5], 0, v[6:7]
	global_load_dwordx4 v[152:155], v[4:5], off
	global_load_dwordx4 v[156:159], v[4:5], off offset:16
	v_and_b32_e32 v4, 60, v0
	v_lshlrev_b32_e32 v5, 2, v0
	s_add_u32 s0, s0, 8
	s_movk_i32 s5, 0xa00
	v_lshlrev_b32_e32 v184, 7, v4
	v_or_b32_e32 v4, 64, v4
	v_bitop3_b32 v195, v5, v6, 48 bitop3:0x6c
	v_lshl_add_u64 v[178:179], s[14:15], 0, v[170:171]
	v_lshl_add_u64 v[180:181], s[16:17], 0, v[2:3]
	s_addc_u32 s1, s1, 0
	v_mad_u32_u24 v1, v1, s5, 0
	v_lshrrev_b32_e32 v2, 3, v0
	s_movk_i32 s5, 0x50
	v_and_b32_e32 v170, 48, v169
	v_bfe_u32 v0, v0, 2, 4
	v_lshrrev_b32_e32 v5, 2, v4
	v_mov_b32_e32 v144, 0x38383838
	v_lshl_add_u64 v[182:183], s[18:19], 0, v[6:7]
	v_and_b32_e32 v2, 4, v2
	v_mad_u32_u24 v3, v168, s5, v1
	s_add_u32 s12, s12, 0x4900000
	v_add_u32_e32 v1, v1, v170
	v_mul_u32_u24_e32 v0, 0x50, v0
	v_mul_u32_u24_e32 v5, 0x50, v5
	s_movk_i32 s18, 0xffc0
	v_lshlrev_b32_e32 v199, 6, v168
	s_mov_b32 s7, 0
	s_movk_i32 s3, 0x2000
	s_movk_i32 s33, 0x4000
	v_mov_b32_e32 v173, 0x74747474
	v_mov_b32_e32 v194, 0x7f7f7f7f
	v_mov_b32_e32 v145, v144
	v_mov_b32_e32 v146, v144
	v_mov_b32_e32 v147, v144
	v_mov_b32_e32 v148, v144
	v_mov_b32_e32 v149, v144
	v_mov_b32_e32 v150, v144
	v_mov_b32_e32 v151, v144
	s_addc_u32 s13, s13, 0
	v_mov_b32_e32 v185, v171
	v_lshlrev_b32_e32 v186, 7, v4
	v_mov_b32_e32 v187, v171
	s_mov_b64 s[30:31], -1
	s_mov_b64 s[14:15], 0x3000
	s_mov_b64 s[16:17], 0xc0
	s_mov_b32 s19, -1
	s_mov_b32 s5, 0xff61b1e6
	s_mov_b32 s36, 0x41000000
	s_mov_b64 s[20:21], 0x80
	s_mov_b64 s[22:23], 0x11000
	s_mov_b64 s[24:25], 0x400
	s_mov_b64 s[26:27], 0x440
	s_mov_b32 s37, 0x42800000
	v_add_u32_e32 v196, v3, v2
	v_add_u32_e32 v197, v1, v0
	v_add_u32_e32 v198, v1, v5
	v_add_u32_e32 v197, 0x10000, v197
	v_add_u32_e32 v198, 0x10000, v198
	v_mov_b32_e32 v0, v171
	v_mov_b32_e32 v1, v171
	v_mov_b32_e32 v2, v171
	v_mov_b32_e32 v3, v171
	v_mov_b32_e32 v4, v171
	v_mov_b32_e32 v5, v171
	v_mov_b32_e32 v6, v171
	v_mov_b32_e32 v8, v171
	v_mov_b32_e32 v9, v171
	v_mov_b32_e32 v10, v171
	v_mov_b32_e32 v11, v171
	v_mov_b32_e32 v12, v171
	v_mov_b32_e32 v13, v171
	v_mov_b32_e32 v14, v171
	v_mov_b32_e32 v15, v171
	s_mov_b32 s38, 0
	v_mov_b32_e32 v160, v171
	v_mov_b32_e32 v161, v171
	v_mov_b32_e32 v162, v171
	v_mov_b32_e32 v163, v171
	v_mov_b32_e32 v164, v171
	v_mov_b32_e32 v165, v171
	v_mov_b32_e32 v166, v171
	v_mov_b32_e32 v167, v171
	v_xor_b32_e32 v200, 16, v195
	v_add_u32_e32 v201, 0, v199
	v_add_u32_e32 v222, v199, v195
	v_add_u32_e32 v223, v199, v200
	v_readfirstlane_b32 s40, v169
	v_add_u32_e32 v224, 0x8000, v222
	v_add_u32_e32 v225, 0x8000, v223
	v_mov_b32_e32 v202, 0x12000
	s_branch .LBB3_3
.LBB3_1:
	s_load_dword s6, s[0:1], 0x0
	s_waitcnt lgkmcnt(0)
	s_add_i32 s2, s6, s2
	s_ashr_i32 s30, s2, 3
	s_ashr_i32 s31, s30, 31
	s_lshr_b32 s31, s31, 29
	s_lshl_b32 s6, s2, 4
	s_add_i32 s31, s30, s31
	s_and_b32 s6, s6, 0x70
	s_ashr_i32 s34, s31, 3
	s_and_b32 s31, s31, 0x1fffff8
	s_add_i32 s34, s6, s34
	s_mul_i32 s54, s34, 0x12000
	s_mul_hi_i32 s55, s34, 0x12000
	s_add_u32 s46, s50, s54
	s_addc_u32 s47, s51, s55
	s_add_u32 s48, s52, s54
	s_addc_u32 s49, s53, s55
	s_sub_i32 s6, s30, s31
	v_lshl_or_b32 v80, s6, 7, v192
	s_add_u32 s6, s40, 0x0
	v_mad_i64_i32 v[174:175], s[30:31], s34, v202, v[178:179]
	s_mov_b32 m0, s6
	s_add_u32 s6, s40, 0x8000
	v_mad_i64_i32 v[176:177], s[30:31], s34, v202, v[180:181]
	global_load_lds_dwordx4 v[174:175], off
	s_mov_b32 m0, s6
	s_add_u32 s6, s40, 0x2000
	global_load_lds_dwordx4 v[176:177], off
	v_lshl_add_u64 v[82:83], v[174:175], 0, s[8:9]
	s_mov_b32 m0, s6
	s_add_u32 s6, s40, 0x4000
	s_ashr_i32 s35, s34, 31
	global_load_lds_dwordx4 v[82:83], off
	v_lshl_add_u64 v[82:83], v[174:175], 0, s[10:11]
	s_mov_b32 m0, s6
	s_add_u32 s6, s40, 0xa000
	global_load_lds_dwordx4 v[82:83], off
	v_lshl_add_u64 v[82:83], v[176:177], 0, 64
	s_mov_b32 m0, s6
	s_lshl_b64 s[30:31], s[34:35], 10
	v_ashrrev_i32_e32 v81, 31, v80
	global_load_lds_dwordx4 v[82:83], off
	v_lshl_add_u64 v[82:83], s[30:31], 0, v[80:81]
	v_or_b32_e32 v82, v82, v168
	v_lshlrev_b64 v[82:83], 6, v[82:83]
	v_lshl_add_u64 v[82:83], v[182:183], 0, v[82:83]
	global_load_dwordx4 v[152:155], v[82:83], off
	global_load_dwordx4 v[156:159], v[82:83], off offset:16
.LBB3_2:
	v_exp_f32_e32 v81, v112
	v_exp_f32_e32 v82, v113
	v_exp_f32_e32 v85, v116
	v_exp_f32_e32 v86, v117
	v_exp_f32_e32 v89, v120
	v_exp_f32_e32 v90, v121
	v_exp_f32_e32 v93, v124
	v_exp_f32_e32 v94, v125
	v_exp_f32_e32 v64, v64
	v_exp_f32_e32 v65, v65
	v_exp_f32_e32 v68, v68
	v_exp_f32_e32 v69, v69
	v_exp_f32_e32 v72, v72
	v_exp_f32_e32 v73, v73
	v_exp_f32_e32 v76, v76
	v_exp_f32_e32 v77, v77
	v_exp_f32_e32 v83, v114
	v_exp_f32_e32 v84, v115
	v_exp_f32_e32 v87, v118
	v_exp_f32_e32 v88, v119
	v_exp_f32_e32 v91, v122
	v_exp_f32_e32 v92, v123
	v_exp_f32_e32 v95, v126
	v_exp_f32_e32 v96, v127
	v_exp_f32_e32 v66, v66
	v_exp_f32_e32 v67, v67
	v_exp_f32_e32 v70, v70
	v_exp_f32_e32 v71, v71
	v_exp_f32_e32 v74, v74
	v_exp_f32_e32 v75, v75
	v_exp_f32_e32 v78, v78
	v_exp_f32_e32 v79, v79
	v_cvt_pk_fp8_f32 v160, v81, v82
	v_cvt_pk_fp8_f32 v161, v85, v86
	v_cvt_pk_fp8_f32 v162, v89, v90
	v_cvt_pk_fp8_f32 v163, v93, v94
	v_cvt_pk_fp8_f32 v164, v64, v65
	v_cvt_pk_fp8_f32 v165, v68, v69
	v_cvt_pk_fp8_f32 v166, v72, v73
	v_cvt_pk_fp8_f32 v167, v76, v77
	v_cvt_pk_fp8_f32 v160, v83, v84 op_sel:[0,0,1]
	v_cvt_pk_fp8_f32 v161, v87, v88 op_sel:[0,0,1]
	v_cvt_pk_fp8_f32 v162, v91, v92 op_sel:[0,0,1]
	v_cvt_pk_fp8_f32 v163, v95, v96 op_sel:[0,0,1]
	v_cvt_pk_fp8_f32 v164, v66, v67 op_sel:[0,0,1]
	v_cvt_pk_fp8_f32 v165, v70, v71 op_sel:[0,0,1]
	v_cvt_pk_fp8_f32 v166, v74, v75 op_sel:[0,0,1]
	v_cvt_pk_fp8_f32 v167, v78, v79 op_sel:[0,0,1]
	s_lshl_b32 s6, s4, 7
	s_and_b32 s6, s6, 0xfffffc00
	v_mfma_scale_f32_32x32x64_f8f6f4 v[48:63], v[144:151], v[160:167], v[48:63], v194, v194 op_sel_hi:[0,0,0]
	s_nop 15
	s_nop 3
	s_lshl_b32 s4, s4, 6
	v_mul_f32_e32 v48, 0x41800000, v48
	s_waitcnt lgkmcnt(0)
	v_mfma_scale_f32_32x32x64_f8f6f4 v[32:47], v[128:135], v[160:167], v[32:47], v194, v194 op_sel_hi:[0,0,0]
	v_div_scale_f32 v49, s[30:31], v48, v48, s37
	v_rcp_f32_e32 v66, v49
	s_mov_b64 s[30:31], 0
	v_fma_f32 v50, -v49, v66, 1.0
	v_fmac_f32_e32 v66, v50, v66
	v_div_scale_f32 v50, vcc, s37, v48, s37
	v_mul_f32_e32 v51, v50, v66
	v_fma_f32 v52, -v49, v51, v50
	v_fmac_f32_e32 v51, v52, v66
	v_fma_f32 v49, -v49, v51, v50
	v_div_fmas_f32 v49, v49, v66, v51
	v_mfma_scale_f32_32x32x64_f8f6f4 v[16:31], v[136:143], v[160:167], v[16:31], v194, v194 op_sel_hi:[0,0,0]
	v_div_fixup_f32 v48, v49, v48, s37
	s_nop 6
	v_mul_f32_e32 v32, v48, v32
	v_mul_f32_e32 v33, v48, v33
	v_mov_b32_e32 v49, 0
	v_cvt_pk_fp8_f32 v49, v32, v33
	v_mul_f32_e32 v32, v48, v34
	v_mul_f32_e32 v33, v48, v35
	s_and_b64 vcc, exec, s[28:29]
	v_cvt_pk_fp8_f32 v49, v32, v33 op_sel:[0,0,1]
	v_mov_b32_e32 v32, 0
	v_mov_b32_e32 v33, 0
	s_nop 1
	v_mul_f32_e32 v16, v48, v16
	v_mul_f32_e32 v17, v48, v17
	v_cvt_pk_fp8_f32 v32, v16, v17
	v_mul_f32_e32 v16, v48, v36
	v_mul_f32_e32 v17, v48, v37
	v_cvt_pk_fp8_f32 v33, v16, v17
	v_mul_f32_e32 v18, v48, v18
	v_mul_f32_e32 v19, v48, v19
	v_mul_f32_e32 v16, v48, v38
	v_mul_f32_e32 v17, v48, v39
	v_cvt_pk_fp8_f32 v32, v18, v19 op_sel:[0,0,1]
	v_cvt_pk_fp8_f32 v33, v16, v17 op_sel:[0,0,1]
	v_mul_f32_e32 v16, v48, v20
	v_mul_f32_e32 v17, v48, v21
	v_mov_b32_e32 v18, 0
	v_cvt_pk_fp8_f32 v18, v16, v17
	v_mul_f32_e32 v17, v48, v22
	v_mul_f32_e32 v19, v48, v23
	v_mov_b32_e32 v22, 0
	v_cvt_pk_fp8_f32 v18, v17, v19 op_sel:[0,0,1]
	v_mul_f32_e32 v17, v48, v40
	v_mul_f32_e32 v19, v48, v41
	v_cvt_pk_fp8_f32 v22, v17, v19
	v_mul_f32_e32 v17, v48, v24
	v_mul_f32_e32 v19, v48, v25
	v_mov_b32_e32 v23, 0
	v_cvt_pk_fp8_f32 v23, v17, v19
	v_mul_f32_e32 v17, v48, v26
	v_mul_f32_e32 v19, v48, v27
	v_mov_b32_e32 v24, 0
	v_cvt_pk_fp8_f32 v23, v17, v19 op_sel:[0,0,1]
	v_mul_f32_e32 v17, v48, v44
	v_mul_f32_e32 v19, v48, v45
	v_cvt_pk_fp8_f32 v24, v17, v19
	v_mul_f32_e32 v17, v48, v28
	v_mul_f32_e32 v19, v48, v29
	v_mov_b32_e32 v25, 0
	v_cvt_pk_fp8_f32 v25, v17, v19
	v_mul_f32_e32 v20, v48, v42
	v_mul_f32_e32 v21, v48, v43
	v_cvt_pk_fp8_f32 v22, v20, v21 op_sel:[0,0,1]
	v_mul_f32_e32 v20, v48, v46
	v_mul_f32_e32 v21, v48, v47
	v_cvt_pk_fp8_f32 v24, v20, v21 op_sel:[0,0,1]
	v_mul_f32_e32 v17, v48, v30
	v_mul_f32_e32 v19, v48, v31
	v_add_u32_e32 v16, 0x10000, v196
	v_cvt_pk_fp8_f32 v25, v17, v19 op_sel:[0,0,1]
	ds_write2_b32 v16, v49, v33 offset1:2
	ds_write2_b32 v16, v32, v18 offset0:8 offset1:10
	ds_write2_b32 v16, v22, v24 offset0:4 offset1:6
	ds_write2_b32 v16, v23, v25 offset0:12 offset1:14
	v_add_u32_e32 v16, s6, v172
	v_ashrrev_i32_e32 v17, 31, v16
	s_waitcnt lgkmcnt(0)
	v_lshlrev_b64 v[16:17], 9, v[16:17]
	v_lshl_add_u64 v[20:21], s[12:13], 0, v[16:17]
	s_and_b32 s6, s4, 0x1c0
	ds_read_b128 v[16:19], v197
	v_lshl_add_u64 v[24:25], v[20:21], 0, s[6:7]
	ds_read_b128 v[20:23], v198
	v_lshl_add_u64 v[24:25], v[24:25], 0, v[170:171]
	v_lshl_add_u64 v[26:27], v[24:25], 0, v[184:185]
	s_waitcnt lgkmcnt(0)
	global_store_dwordx4 v[26:27], v[16:19], off
	s_mov_b32 s4, s34
	v_mov_b32_e32 v172, v80
	v_lshl_add_u64 v[16:17], v[24:25], 0, v[186:187]
	global_store_dwordx4 v[16:17], v[20:23], off
	s_waitcnt lgkmcnt(0)
	s_cbranch_vccnz .LBB3_18
.LBB3_3:
	s_add_u32 s42, s46, 0x3000
	s_addc_u32 s43, s47, 0
	s_add_u32 s44, s48, 0x40
	s_addc_u32 s45, s49, 0
	v_mov_b64_e32 v[30:31], v[14:15]
	v_mov_b64_e32 v[28:29], v[12:13]
	v_mov_b64_e32 v[26:27], v[10:11]
	v_mov_b64_e32 v[24:25], v[8:9]
	v_mov_b64_e32 v[22:23], v[6:7]
	v_mov_b64_e32 v[20:21], v[4:5]
	v_mov_b64_e32 v[18:19], v[2:3]
	v_mov_b64_e32 v[16:17], v[0:1]
	v_add_u32_e32 v32, s38, v201
	s_waitcnt vmcnt(0) lgkmcnt(0)
	s_barrier
	v_add_u32_e32 v41, v32, v200
	v_add_u32_e32 v40, v32, v195
	ds_read_b128 v[36:39], v41
	ds_read_b128 v[32:35], v40
	ds_read_b128 v[48:51], v40 offset:2048
	ds_read_b128 v[52:55], v41 offset:2048
	s_waitcnt vmcnt(0) lgkmcnt(0)
	v_mfma_scale_f32_32x32x64_f8f6f4 v[32:47], v[32:39], v[152:159], v[16:31], v173, v194 op_sel_hi:[0,0,0]
	s_waitcnt vmcnt(2) lgkmcnt(0)
	s_barrier
	s_xor_b64 s[28:29], s[30:31], -1
	s_mov_b32 s6, -1
	s_nop 15
	v_max_f32_e32 v56, v33, v33
	v_mfma_scale_f32_32x32x64_f8f6f4 v[16:31], v[48:55], v[152:159], v[16:31], v173, v194 op_sel_hi:[0,0,0]
	v_max_f32_e32 v57, v32, v32
	v_max_f32_e32 v56, v57, v56
	s_nop 15
	s_nop 1
	v_max3_f32 v48, v34, v35, v17
	v_max3_f32 v49, v56, v16, v18
	v_max3_f32 v49, v49, v19, v36
	v_max3_f32 v48, v48, v38, v39
	v_max3_f32 v48, v48, v22, v23
	v_max3_f32 v49, v49, v37, v20
	v_max3_f32 v48, v48, v42, v43
	v_max3_f32 v49, v49, v21, v40
	v_max3_f32 v48, v48, v26, v27
	v_max3_f32 v49, v49, v41, v24
	v_max3_f32 v48, v48, v46, v47
	v_max3_f32 v49, v49, v25, v44
	v_max3_f32 v48, v48, v30, v31
	v_max3_f32 v49, v49, v45, v28
	v_max3_f32 v48, v49, v29, v48
	v_mov_b32_e32 v49, v48
	s_nop 1
	v_permlane32_swap_b32_e32 v48, v49
	v_max_f32_e32 v49, v49, v49
	v_max_f32_e32 v48, v48, v48
	v_max_f32_e32 v48, v48, v49
	v_sub_f32_e32 v95, v47, v48
	v_sub_f32_e32 v94, v46, v48
	v_sub_f32_e32 v93, v45, v48
	v_sub_f32_e32 v92, v44, v48
	v_sub_f32_e32 v91, v43, v48
	v_sub_f32_e32 v90, v42, v48
	v_sub_f32_e32 v89, v41, v48
	v_sub_f32_e32 v88, v40, v48
	v_sub_f32_e32 v87, v39, v48
	v_sub_f32_e32 v86, v38, v48
	v_sub_f32_e32 v85, v37, v48
	v_sub_f32_e32 v84, v36, v48
	v_sub_f32_e32 v83, v35, v48
	v_sub_f32_e32 v82, v34, v48
	v_sub_f32_e32 v81, v33, v48
	v_sub_f32_e32 v80, v32, v48
	v_sub_f32_e32 v111, v31, v48
	v_sub_f32_e32 v110, v30, v48
	v_sub_f32_e32 v109, v29, v48
	v_sub_f32_e32 v108, v28, v48
	v_sub_f32_e32 v107, v27, v48
	v_sub_f32_e32 v106, v26, v48
	v_sub_f32_e32 v105, v25, v48
	v_sub_f32_e32 v104, v24, v48
	v_sub_f32_e32 v103, v23, v48
	v_sub_f32_e32 v102, v22, v48
	v_sub_f32_e32 v101, v21, v48
	v_sub_f32_e32 v100, v20, v48
	v_sub_f32_e32 v99, v19, v48
	v_sub_f32_e32 v98, v18, v48
	v_sub_f32_e32 v97, v17, v48
	v_sub_f32_e32 v96, v16, v48
	v_xor_b32_e32 v64, 0x80000000, v48
	v_mov_b64_e32 v[46:47], v[14:15]
	v_mov_b64_e32 v[30:31], v[14:15]
	v_mov_b64_e32 v[62:63], v[14:15]
	v_mov_b32_e32 v65, v64
	v_mov_b32_e32 v66, v64
	v_mov_b32_e32 v67, v64
	v_mov_b32_e32 v68, v64
	v_mov_b32_e32 v69, v64
	v_mov_b32_e32 v70, v64
	v_mov_b32_e32 v71, v64
	v_mov_b32_e32 v72, v64
	v_mov_b32_e32 v73, v64
	v_mov_b32_e32 v74, v64
	v_mov_b32_e32 v75, v64
	v_mov_b32_e32 v76, v64
	v_mov_b32_e32 v77, v64
	v_mov_b32_e32 v78, v64
	v_mov_b32_e32 v79, v64
	v_mov_b64_e32 v[44:45], v[12:13]
	v_mov_b64_e32 v[42:43], v[10:11]
	v_mov_b64_e32 v[40:41], v[8:9]
	v_mov_b64_e32 v[38:39], v[6:7]
	v_mov_b64_e32 v[36:37], v[4:5]
	v_mov_b64_e32 v[34:35], v[2:3]
	v_mov_b64_e32 v[32:33], v[0:1]
	v_mov_b64_e32 v[28:29], v[12:13]
	v_mov_b64_e32 v[26:27], v[10:11]
	v_mov_b64_e32 v[24:25], v[8:9]
	v_mov_b64_e32 v[22:23], v[6:7]
	v_mov_b64_e32 v[20:21], v[4:5]
	v_mov_b64_e32 v[18:19], v[2:3]
	v_mov_b64_e32 v[16:17], v[0:1]
	v_mov_b64_e32 v[60:61], v[12:13]
	v_mov_b64_e32 v[58:59], v[10:11]
	v_mov_b64_e32 v[56:57], v[8:9]
	v_mov_b64_e32 v[54:55], v[6:7]
	v_mov_b64_e32 v[52:53], v[4:5]
	v_mov_b64_e32 v[50:51], v[2:3]
	v_mov_b64_e32 v[48:49], v[0:1]
	s_mov_b32 s39, 0
.Lat_loop:
	s_add_u32 m0, s40, 0x6000
	s_nop 0
	global_load_lds_dwordx4 v220, s[42:43]
	s_add_u32 s42, s42, 0x1000
	s_addc_u32 s43, s43, 0
	s_add_u32 m0, s40, 0x0
	s_nop 0
	global_load_lds_dwordx4 v220, s[42:43]
	s_add_u32 s42, s42, 0x1000
	s_addc_u32 s43, s43, 0
	ds_read_b128 v[112:115], v222 offset:8192
	ds_read_b128 v[128:131], v222 offset:10240
	ds_read_b128 v[116:119], v223 offset:8192
	ds_read_b128 v[132:135], v223 offset:10240
	s_setprio 1
	v_exp_f32_e32 v80, v80
	v_exp_f32_e32 v81, v81
	v_exp_f32_e32 v82, v82
	v_exp_f32_e32 v83, v83
	v_exp_f32_e32 v84, v84
	v_exp_f32_e32 v85, v85
	v_exp_f32_e32 v86, v86
	v_exp_f32_e32 v87, v87
	s_waitcnt lgkmcnt(0)
	v_mfma_scale_f32_32x32x64_f8f6f4 v[112:127], v[112:119], v[152:159], v[64:79], v173, v194 op_sel_hi:[0,0,0]
	v_cvt_pk_fp8_f32 v160, v80, v81
	v_cvt_pk_fp8_f32 v161, v84, v85
	v_exp_f32_e32 v88, v88
	v_exp_f32_e32 v89, v89
	v_cvt_pk_fp8_f32 v160, v82, v83 op_sel:[0,0,1]
	v_cvt_pk_fp8_f32 v161, v86, v87 op_sel:[0,0,1]
	v_exp_f32_e32 v90, v90
	v_exp_f32_e32 v91, v91
	v_exp_f32_e32 v92, v92
	v_exp_f32_e32 v93, v93
	v_exp_f32_e32 v94, v94
	v_exp_f32_e32 v95, v95
	s_setprio 0
	ds_read_b128 v[80:83], v224 offset:0
	ds_read_b128 v[212:215], v224 offset:2048
	ds_read_b128 v[84:87], v225 offset:0
	ds_read_b128 v[216:219], v225 offset:2048
	v_cvt_pk_fp8_f32 v162, v88, v89
	v_cvt_pk_fp8_f32 v163, v92, v93
	v_exp_f32_e32 v96, v96
	v_exp_f32_e32 v97, v97
	v_cvt_pk_fp8_f32 v162, v90, v91 op_sel:[0,0,1]
	v_cvt_pk_fp8_f32 v163, v94, v95 op_sel:[0,0,1]
	v_exp_f32_e32 v98, v98
	v_exp_f32_e32 v99, v99
	v_exp_f32_e32 v100, v100
	v_exp_f32_e32 v101, v101
	v_exp_f32_e32 v102, v102
	v_exp_f32_e32 v103, v103
	v_mfma_scale_f32_32x32x64_f8f6f4 v[128:143], v[128:135], v[152:159], v[64:79], v173, v194 op_sel_hi:[0,0,0]
	v_cvt_pk_fp8_f32 v164, v96, v97
	v_cvt_pk_fp8_f32 v165, v100, v101
	v_exp_f32_e32 v104, v104
	v_exp_f32_e32 v105, v105
	v_cvt_pk_fp8_f32 v164, v98, v99 op_sel:[0,0,1]
	v_cvt_pk_fp8_f32 v165, v102, v103 op_sel:[0,0,1]
	v_exp_f32_e32 v106, v106
	v_exp_f32_e32 v107, v107
	v_exp_f32_e32 v108, v108
	v_exp_f32_e32 v109, v109
	v_exp_f32_e32 v110, v110
	v_exp_f32_e32 v111, v111
	s_nop 0
	v_cvt_pk_fp8_f32 v166, v104, v105
	v_cvt_pk_fp8_f32 v167, v108, v109
	v_cvt_pk_fp8_f32 v166, v106, v107 op_sel:[0,0,1]
	v_cvt_pk_fp8_f32 v167, v110, v111 op_sel:[0,0,1]
	s_setprio 1
	s_waitcnt lgkmcnt(0)
	v_mfma_scale_f32_32x32x64_f8f6f4 v[32:47], v[80:87], v[160:167], v[32:47], v194, v194 op_sel_hi:[0,0,0]
	v_max3_f32 v88, v112, s5, v113
	v_max3_f32 v88, v88, v114, v115
	v_max3_f32 v88, v88, v116, v117
	v_max3_f32 v88, v88, v118, v119
	v_max3_f32 v88, v88, v120, v121
	v_max3_f32 v88, v88, v122, v123
	v_max3_f32 v88, v88, v124, v125
	v_max3_f32 v88, v88, v126, v127
	s_add_u32 s44, s44, 64
	s_addc_u32 s45, s45, 0
	s_add_u32 m0, s40, 0xc000
	s_nop 0
	global_load_lds_dwordx4 v221, s[44:45]
	v_mfma_scale_f32_32x32x64_f8f6f4 v[16:31], v[212:219], v[160:167], v[16:31], v194, v194 op_sel_hi:[0,0,0]
	v_max3_f32 v80, v128, s5, v129
	v_max3_f32 v80, v80, v130, v131
	v_max3_f32 v80, v80, v132, v133
	v_max3_f32 v80, v80, v134, v135
	v_max3_f32 v80, v80, v136, v137
	v_max3_f32 v80, v80, v138, v139
	v_max3_f32 v80, v80, v140, v141
	v_max3_f32 v80, v80, v142, v143
	s_add_u32 s44, s44, 64
	s_addc_u32 s45, s45, 0
	s_add_u32 m0, s40, 0xe000
	s_nop 0
	global_load_lds_dwordx4 v221, s[44:45]
	v_mfma_scale_f32_32x32x64_f8f6f4 v[48:63], v[144:151], v[160:167], v[48:63], v194, v194 op_sel_hi:[0,0,0]
	s_setprio 0
	v_max_f32_e32 v80, v88, v80
	v_cmp_lt_f32_e32 vcc, s36, v80
	s_cbranch_vccnz .Lat_rare_L1
.Lat_back_L1:
	ds_read_b128 v[80:83], v222 offset:16384
	ds_read_b128 v[96:99], v222 offset:18432
	ds_read_b128 v[84:87], v223 offset:16384
	ds_read_b128 v[100:103], v223 offset:18432
	s_setprio 1
	v_exp_f32_e32 v112, v112
	v_exp_f32_e32 v113, v113
	v_exp_f32_e32 v114, v114
	v_exp_f32_e32 v115, v115
	v_exp_f32_e32 v116, v116
	v_exp_f32_e32 v117, v117
	v_exp_f32_e32 v118, v118
	v_exp_f32_e32 v119, v119
	s_waitcnt lgkmcnt(0)
	v_mfma_scale_f32_32x32x64_f8f6f4 v[80:95], v[80:87], v[152:159], v[64:79], v173, v194 op_sel_hi:[0,0,0]
	v_cvt_pk_fp8_f32 v160, v112, v113
	v_cvt_pk_fp8_f32 v161, v116, v117
	v_exp_f32_e32 v120, v120
	v_exp_f32_e32 v121, v121
	v_cvt_pk_fp8_f32 v160, v114, v115 op_sel:[0,0,1]
	v_cvt_pk_fp8_f32 v161, v118, v119 op_sel:[0,0,1]
	v_exp_f32_e32 v122, v122
	v_exp_f32_e32 v123, v123
	v_exp_f32_e32 v124, v124
	v_exp_f32_e32 v125, v125
	v_exp_f32_e32 v126, v126
	v_exp_f32_e32 v127, v127
	s_setprio 0
	ds_read_b128 v[112:115], v224 offset:8192
	ds_read_b128 v[212:215], v224 offset:10240
	ds_read_b128 v[116:119], v225 offset:8192
	ds_read_b128 v[216:219], v225 offset:10240
	v_cvt_pk_fp8_f32 v162, v120, v121
	v_cvt_pk_fp8_f32 v163, v124, v125
	v_exp_f32_e32 v128, v128
	v_exp_f32_e32 v129, v129
	v_cvt_pk_fp8_f32 v162, v122, v123 op_sel:[0,0,1]
	v_cvt_pk_fp8_f32 v163, v126, v127 op_sel:[0,0,1]
	v_exp_f32_e32 v130, v130
	v_exp_f32_e32 v131, v131
	v_exp_f32_e32 v132, v132
	v_exp_f32_e32 v133, v133
	v_exp_f32_e32 v134, v134
	v_exp_f32_e32 v135, v135
	v_mfma_scale_f32_32x32x64_f8f6f4 v[96:111], v[96:103], v[152:159], v[64:79], v173, v194 op_sel_hi:[0,0,0]
	v_cvt_pk_fp8_f32 v164, v128, v129
	v_cvt_pk_fp8_f32 v165, v132, v133
	v_exp_f32_e32 v136, v136
	v_exp_f32_e32 v137, v137
	v_cvt_pk_fp8_f32 v164, v130, v131 op_sel:[0,0,1]
	v_cvt_pk_fp8_f32 v165, v134, v135 op_sel:[0,0,1]
	v_exp_f32_e32 v138, v138
	v_exp_f32_e32 v139, v139
	v_exp_f32_e32 v140, v140
	v_exp_f32_e32 v141, v141
	v_exp_f32_e32 v142, v142
	v_exp_f32_e32 v143, v143
	s_nop 0
	v_cvt_pk_fp8_f32 v166, v136, v137
	v_cvt_pk_fp8_f32 v167, v140, v141
	v_cvt_pk_fp8_f32 v166, v138, v139 op_sel:[0,0,1]
	v_cvt_pk_fp8_f32 v167, v142, v143 op_sel:[0,0,1]
	s_setprio 1
	s_waitcnt lgkmcnt(0)
	v_mfma_scale_f32_32x32x64_f8f6f4 v[32:47], v[112:119], v[160:167], v[32:47], v194, v194 op_sel_hi:[0,0,0]
	v_max3_f32 v120, v80, s5, v81
	v_max3_f32 v120, v120, v82, v83
	v_max3_f32 v120, v120, v84, v85
	v_max3_f32 v120, v120, v86, v87
	v_max3_f32 v120, v120, v88, v89
	v_max3_f32 v120, v120, v90, v91
	v_max3_f32 v120, v120, v92, v93
	v_max3_f32 v120, v120, v94, v95
	v_mfma_scale_f32_32x32x64_f8f6f4 v[16:31], v[212:219], v[160:167], v[16:31], v194, v194 op_sel_hi:[0,0,0]
	v_max3_f32 v112, v96, s5, v97
	v_max3_f32 v112, v112, v98, v99
	v_max3_f32 v112, v112, v100, v101
	v_max3_f32 v112, v112, v102, v103
	v_max3_f32 v112, v112, v104, v105
	v_max3_f32 v112, v112, v106, v107
	v_max3_f32 v112, v112, v108, v109
	v_max3_f32 v112, v112, v110, v111
	v_mfma_scale_f32_32x32x64_f8f6f4 v[48:63], v[144:151], v[160:167], v[48:63], v194, v194 op_sel_hi:[0,0,0]
	s_setprio 0
	v_max_f32_e32 v112, v120, v112
	v_cmp_lt_f32_e32 vcc, s36, v112
	s_cbranch_vccnz .Lat_rare_L2
.Lat_back_L2:
	s_waitcnt vmcnt(0) lgkmcnt(0)
	s_barrier
	s_add_u32 m0, s40, 0x2000
	s_nop 0
	global_load_lds_dwordx4 v220, s[42:43]
	s_add_u32 s42, s42, 0x1000
	s_addc_u32 s43, s43, 0
	s_add_u32 m0, s40, 0x4000
	s_nop 0
	global_load_lds_dwordx4 v220, s[42:43]
	s_add_u32 s42, s42, 0x1000
	s_addc_u32 s43, s43, 0
	ds_read_b128 v[112:115], v222 offset:24576
	ds_read_b128 v[128:131], v222 offset:26624
	ds_read_b128 v[116:119], v223 offset:24576
	ds_read_b128 v[132:135], v223 offset:26624
	s_setprio 1
	v_exp_f32_e32 v80, v80
	v_exp_f32_e32 v81, v81
	v_exp_f32_e32 v82, v82
	v_exp_f32_e32 v83, v83
	v_exp_f32_e32 v84, v84
	v_exp_f32_e32 v85, v85
	v_exp_f32_e32 v86, v86
	v_exp_f32_e32 v87, v87
	s_waitcnt lgkmcnt(0)
	v_mfma_scale_f32_32x32x64_f8f6f4 v[112:127], v[112:119], v[152:159], v[64:79], v173, v194 op_sel_hi:[0,0,0]
	v_cvt_pk_fp8_f32 v160, v80, v81
	v_cvt_pk_fp8_f32 v161, v84, v85
	v_exp_f32_e32 v88, v88
	v_exp_f32_e32 v89, v89
	v_cvt_pk_fp8_f32 v160, v82, v83 op_sel:[0,0,1]
	v_cvt_pk_fp8_f32 v161, v86, v87 op_sel:[0,0,1]
	v_exp_f32_e32 v90, v90
	v_exp_f32_e32 v91, v91
	v_exp_f32_e32 v92, v92
	v_exp_f32_e32 v93, v93
	v_exp_f32_e32 v94, v94
	v_exp_f32_e32 v95, v95
	s_setprio 0
	ds_read_b128 v[80:83], v224 offset:16384
	ds_read_b128 v[212:215], v224 offset:18432
	ds_read_b128 v[84:87], v225 offset:16384
	ds_read_b128 v[216:219], v225 offset:18432
	v_cvt_pk_fp8_f32 v162, v88, v89
	v_cvt_pk_fp8_f32 v163, v92, v93
	v_exp_f32_e32 v96, v96
	v_exp_f32_e32 v97, v97
	v_cvt_pk_fp8_f32 v162, v90, v91 op_sel:[0,0,1]
	v_cvt_pk_fp8_f32 v163, v94, v95 op_sel:[0,0,1]
	v_exp_f32_e32 v98, v98
	v_exp_f32_e32 v99, v99
	v_exp_f32_e32 v100, v100
	v_exp_f32_e32 v101, v101
	v_exp_f32_e32 v102, v102
	v_exp_f32_e32 v103, v103
	v_mfma_scale_f32_32x32x64_f8f6f4 v[128:143], v[128:135], v[152:159], v[64:79], v173, v194 op_sel_hi:[0,0,0]
	v_cvt_pk_fp8_f32 v164, v96, v97
	v_cvt_pk_fp8_f32 v165, v100, v101
	v_exp_f32_e32 v104, v104
	v_exp_f32_e32 v105, v105
	v_cvt_pk_fp8_f32 v164, v98, v99 op_sel:[0,0,1]
	v_cvt_pk_fp8_f32 v165, v102, v103 op_sel:[0,0,1]
	v_exp_f32_e32 v106, v106
	v_exp_f32_e32 v107, v107
	v_exp_f32_e32 v108, v108
	v_exp_f32_e32 v109, v109
	v_exp_f32_e32 v110, v110
	v_exp_f32_e32 v111, v111
	s_nop 0
	v_cvt_pk_fp8_f32 v166, v104, v105
	v_cvt_pk_fp8_f32 v167, v108, v109
	v_cvt_pk_fp8_f32 v166, v106, v107 op_sel:[0,0,1]
	v_cvt_pk_fp8_f32 v167, v110, v111 op_sel:[0,0,1]
	s_setprio 1
	s_waitcnt lgkmcnt(0)
	v_mfma_scale_f32_32x32x64_f8f6f4 v[32:47], v[80:87], v[160:167], v[32:47], v194, v194 op_sel_hi:[0,0,0]
	v_max3_f32 v88, v112, s5, v113
	v_max3_f32 v88, v88, v114, v115
	v_max3_f32 v88, v88, v116, v117
	v_max3_f32 v88, v88, v118, v119
	v_max3_f32 v88, v88, v120, v121
	v_max3_f32 v88, v88, v122, v123
	v_max3_f32 v88, v88, v124, v125
	v_max3_f32 v88, v88, v126, v127
	s_add_u32 s44, s44, 64
	s_addc_u32 s45, s45, 0
	s_add_u32 m0, s40, 0x8000
	s_nop 0
	global_load_lds_dwordx4 v221, s[44:45]
	v_mfma_scale_f32_32x32x64_f8f6f4 v[16:31], v[212:219], v[160:167], v[16:31], v194, v194 op_sel_hi:[0,0,0]
	v_max3_f32 v80, v128, s5, v129
	v_max3_f32 v80, v80, v130, v131
	v_max3_f32 v80, v80, v132, v133
	v_max3_f32 v80, v80, v134, v135
	v_max3_f32 v80, v80, v136, v137
	v_max3_f32 v80, v80, v138, v139
	v_max3_f32 v80, v80, v140, v141
	v_max3_f32 v80, v80, v142, v143
	s_add_u32 s44, s44, 64
	s_addc_u32 s45, s45, 0
	s_add_u32 m0, s40, 0xa000
	s_nop 0
	global_load_lds_dwordx4 v221, s[44:45]
	v_mfma_scale_f32_32x32x64_f8f6f4 v[48:63], v[144:151], v[160:167], v[48:63], v194, v194 op_sel_hi:[0,0,0]
	s_setprio 0
	v_max_f32_e32 v80, v88, v80
	v_cmp_lt_f32_e32 vcc, s36, v80
	s_cbranch_vccnz .Lat_rare_L3
.Lat_back_L3:
	ds_read_b128 v[80:83], v222 offset:0
	ds_read_b128 v[96:99], v222 offset:2048
	ds_read_b128 v[84:87], v223 offset:0
	ds_read_b128 v[100:103], v223 offset:2048
	s_setprio 1
	v_exp_f32_e32 v112, v112
	v_exp_f32_e32 v113, v113
	v_exp_f32_e32 v114, v114
	v_exp_f32_e32 v115, v115
	v_exp_f32_e32 v116, v116
	v_exp_f32_e32 v117, v117
	v_exp_f32_e32 v118, v118
	v_exp_f32_e32 v119, v119
	s_waitcnt lgkmcnt(0)
	v_mfma_scale_f32_32x32x64_f8f6f4 v[80:95], v[80:87], v[152:159], v[64:79], v173, v194 op_sel_hi:[0,0,0]
	v_cvt_pk_fp8_f32 v160, v112, v113
	v_cvt_pk_fp8_f32 v161, v116, v117
	v_exp_f32_e32 v120, v120
	v_exp_f32_e32 v121, v121
	v_cvt_pk_fp8_f32 v160, v114, v115 op_sel:[0,0,1]
	v_cvt_pk_fp8_f32 v161, v118, v119 op_sel:[0,0,1]
	v_exp_f32_e32 v122, v122
	v_exp_f32_e32 v123, v123
	v_exp_f32_e32 v124, v124
	v_exp_f32_e32 v125, v125
	v_exp_f32_e32 v126, v126
	v_exp_f32_e32 v127, v127
	s_setprio 0
	ds_read_b128 v[112:115], v224 offset:24576
	ds_read_b128 v[212:215], v224 offset:26624
	ds_read_b128 v[116:119], v225 offset:24576
	ds_read_b128 v[216:219], v225 offset:26624
	v_cvt_pk_fp8_f32 v162, v120, v121
	v_cvt_pk_fp8_f32 v163, v124, v125
	v_exp_f32_e32 v128, v128
	v_exp_f32_e32 v129, v129
	v_cvt_pk_fp8_f32 v162, v122, v123 op_sel:[0,0,1]
	v_cvt_pk_fp8_f32 v163, v126, v127 op_sel:[0,0,1]
	v_exp_f32_e32 v130, v130
	v_exp_f32_e32 v131, v131
	v_exp_f32_e32 v132, v132
	v_exp_f32_e32 v133, v133
	v_exp_f32_e32 v134, v134
	v_exp_f32_e32 v135, v135
	v_mfma_scale_f32_32x32x64_f8f6f4 v[96:111], v[96:103], v[152:159], v[64:79], v173, v194 op_sel_hi:[0,0,0]
	v_cvt_pk_fp8_f32 v164, v128, v129
	v_cvt_pk_fp8_f32 v165, v132, v133
	v_exp_f32_e32 v136, v136
	v_exp_f32_e32 v137, v137
	v_cvt_pk_fp8_f32 v164, v130, v131 op_sel:[0,0,1]
	v_cvt_pk_fp8_f32 v165, v134, v135 op_sel:[0,0,1]
	v_exp_f32_e32 v138, v138
	v_exp_f32_e32 v139, v139
	v_exp_f32_e32 v140, v140
	v_exp_f32_e32 v141, v141
	v_exp_f32_e32 v142, v142
	v_exp_f32_e32 v143, v143
	s_nop 0
	v_cvt_pk_fp8_f32 v166, v136, v137
	v_cvt_pk_fp8_f32 v167, v140, v141
	v_cvt_pk_fp8_f32 v166, v138, v139 op_sel:[0,0,1]
	v_cvt_pk_fp8_f32 v167, v142, v143 op_sel:[0,0,1]
	s_setprio 1
	s_waitcnt lgkmcnt(0)
	v_mfma_scale_f32_32x32x64_f8f6f4 v[32:47], v[112:119], v[160:167], v[32:47], v194, v194 op_sel_hi:[0,0,0]
	v_max3_f32 v120, v80, s5, v81
	v_max3_f32 v120, v120, v82, v83
	v_max3_f32 v120, v120, v84, v85
	v_max3_f32 v120, v120, v86, v87
	v_max3_f32 v120, v120, v88, v89
	v_max3_f32 v120, v120, v90, v91
	v_max3_f32 v120, v120, v92, v93
	v_max3_f32 v120, v120, v94, v95
	v_mfma_scale_f32_32x32x64_f8f6f4 v[16:31], v[212:219], v[160:167], v[16:31], v194, v194 op_sel_hi:[0,0,0]
	v_max3_f32 v112, v96, s5, v97
	v_max3_f32 v112, v112, v98, v99
	v_max3_f32 v112, v112, v100, v101
	v_max3_f32 v112, v112, v102, v103
	v_max3_f32 v112, v112, v104, v105
	v_max3_f32 v112, v112, v106, v107
	v_max3_f32 v112, v112, v108, v109
	v_max3_f32 v112, v112, v110, v111
	v_mfma_scale_f32_32x32x64_f8f6f4 v[48:63], v[144:151], v[160:167], v[48:63], v194, v194 op_sel_hi:[0,0,0]
	s_setprio 0
	v_max_f32_e32 v112, v120, v112
	v_cmp_lt_f32_e32 vcc, s36, v112
	s_cbranch_vccnz .Lat_rare_L4
.Lat_back_L4:
	s_waitcnt vmcnt(0) lgkmcnt(0)
	s_barrier
	s_add_u32 s39, s39, 1
	s_cmp_lt_u32 s39, 3
	s_cbranch_scc1 .Lat_loop
	s_add_u32 m0, s40, 0x6000
	s_nop 0
	global_load_lds_dwordx4 v220, s[42:43]
	s_add_u32 s42, s42, 0x1000
	s_addc_u32 s43, s43, 0
	s_add_u32 m0, s40, 0x0
	s_nop 0
	global_load_lds_dwordx4 v220, s[42:43]
	s_add_u32 s42, s42, 0x1000
	s_addc_u32 s43, s43, 0
	ds_read_b128 v[112:115], v222 offset:8192
	ds_read_b128 v[128:131], v222 offset:10240
	ds_read_b128 v[116:119], v223 offset:8192
	ds_read_b128 v[132:135], v223 offset:10240
	s_setprio 1
	v_exp_f32_e32 v80, v80
	v_exp_f32_e32 v81, v81
	v_exp_f32_e32 v82, v82
	v_exp_f32_e32 v83, v83
	v_exp_f32_e32 v84, v84
	v_exp_f32_e32 v85, v85
	v_exp_f32_e32 v86, v86
	v_exp_f32_e32 v87, v87
	s_waitcnt lgkmcnt(0)
	v_mfma_scale_f32_32x32x64_f8f6f4 v[112:127], v[112:119], v[152:159], v[64:79], v173, v194 op_sel_hi:[0,0,0]
	v_cvt_pk_fp8_f32 v160, v80, v81
	v_cvt_pk_fp8_f32 v161, v84, v85
	v_exp_f32_e32 v88, v88
	v_exp_f32_e32 v89, v89
	v_cvt_pk_fp8_f32 v160, v82, v83 op_sel:[0,0,1]
	v_cvt_pk_fp8_f32 v161, v86, v87 op_sel:[0,0,1]
	v_exp_f32_e32 v90, v90
	v_exp_f32_e32 v91, v91
	v_exp_f32_e32 v92, v92
	v_exp_f32_e32 v93, v93
	v_exp_f32_e32 v94, v94
	v_exp_f32_e32 v95, v95
	s_setprio 0
	ds_read_b128 v[80:83], v224 offset:0
	ds_read_b128 v[212:215], v224 offset:2048
	ds_read_b128 v[84:87], v225 offset:0
	ds_read_b128 v[216:219], v225 offset:2048
	v_cvt_pk_fp8_f32 v162, v88, v89
	v_cvt_pk_fp8_f32 v163, v92, v93
	v_exp_f32_e32 v96, v96
	v_exp_f32_e32 v97, v97
	v_cvt_pk_fp8_f32 v162, v90, v91 op_sel:[0,0,1]
	v_cvt_pk_fp8_f32 v163, v94, v95 op_sel:[0,0,1]
	v_exp_f32_e32 v98, v98
	v_exp_f32_e32 v99, v99
	v_exp_f32_e32 v100, v100
	v_exp_f32_e32 v101, v101
	v_exp_f32_e32 v102, v102
	v_exp_f32_e32 v103, v103
	v_mfma_scale_f32_32x32x64_f8f6f4 v[128:143], v[128:135], v[152:159], v[64:79], v173, v194 op_sel_hi:[0,0,0]
	v_cvt_pk_fp8_f32 v164, v96, v97
	v_cvt_pk_fp8_f32 v165, v100, v101
	v_exp_f32_e32 v104, v104
	v_exp_f32_e32 v105, v105
	v_cvt_pk_fp8_f32 v164, v98, v99 op_sel:[0,0,1]
	v_cvt_pk_fp8_f32 v165, v102, v103 op_sel:[0,0,1]
	v_exp_f32_e32 v106, v106
	v_exp_f32_e32 v107, v107
	v_exp_f32_e32 v108, v108
	v_exp_f32_e32 v109, v109
	v_exp_f32_e32 v110, v110
	v_exp_f32_e32 v111, v111
	s_nop 0
	v_cvt_pk_fp8_f32 v166, v104, v105
	v_cvt_pk_fp8_f32 v167, v108, v109
	v_cvt_pk_fp8_f32 v166, v106, v107 op_sel:[0,0,1]
	v_cvt_pk_fp8_f32 v167, v110, v111 op_sel:[0,0,1]
	s_setprio 1
	s_waitcnt lgkmcnt(0)
	v_mfma_scale_f32_32x32x64_f8f6f4 v[32:47], v[80:87], v[160:167], v[32:47], v194, v194 op_sel_hi:[0,0,0]
	v_max3_f32 v88, v112, s5, v113
	v_max3_f32 v88, v88, v114, v115
	v_max3_f32 v88, v88, v116, v117
	v_max3_f32 v88, v88, v118, v119
	v_max3_f32 v88, v88, v120, v121
	v_max3_f32 v88, v88, v122, v123
	v_max3_f32 v88, v88, v124, v125
	v_max3_f32 v88, v88, v126, v127
	s_add_u32 s44, s44, 64
	s_addc_u32 s45, s45, 0
	s_add_u32 m0, s40, 0xc000
	s_nop 0
	global_load_lds_dwordx4 v221, s[44:45]
	v_mfma_scale_f32_32x32x64_f8f6f4 v[16:31], v[212:219], v[160:167], v[16:31], v194, v194 op_sel_hi:[0,0,0]
	v_max3_f32 v80, v128, s5, v129
	v_max3_f32 v80, v80, v130, v131
	v_max3_f32 v80, v80, v132, v133
	v_max3_f32 v80, v80, v134, v135
	v_max3_f32 v80, v80, v136, v137
	v_max3_f32 v80, v80, v138, v139
	v_max3_f32 v80, v80, v140, v141
	v_max3_f32 v80, v80, v142, v143
	s_add_u32 s44, s44, 64
	s_addc_u32 s45, s45, 0
	s_add_u32 m0, s40, 0xe000
	s_nop 0
	global_load_lds_dwordx4 v221, s[44:45]
	v_mfma_scale_f32_32x32x64_f8f6f4 v[48:63], v[144:151], v[160:167], v[48:63], v194, v194 op_sel_hi:[0,0,0]
	s_setprio 0
	v_max_f32_e32 v80, v88, v80
	v_cmp_lt_f32_e32 vcc, s36, v80
	s_cbranch_vccnz .Lat_rare_P13

.Lat_back_P14:
	s_waitcnt vmcnt(0) lgkmcnt(0)
	s_barrier
	s_add_u32 m0, s40, 0x2000
	s_nop 0
	global_load_lds_dwordx4 v220, s[42:43]
	s_add_u32 s42, s42, 0x1000
	s_addc_u32 s43, s43, 0
	ds_read_b128 v[112:115], v222 offset:24576
	ds_read_b128 v[128:131], v222 offset:26624
	ds_read_b128 v[116:119], v223 offset:24576
	ds_read_b128 v[132:135], v223 offset:26624
	s_setprio 1
	v_exp_f32_e32 v80, v80
	v_exp_f32_e32 v81, v81
	v_exp_f32_e32 v82, v82
	v_exp_f32_e32 v83, v83
	v_exp_f32_e32 v84, v84
	v_exp_f32_e32 v85, v85
	v_exp_f32_e32 v86, v86
	v_exp_f32_e32 v87, v87
	s_waitcnt lgkmcnt(0)
	v_mfma_scale_f32_32x32x64_f8f6f4 v[112:127], v[112:119], v[152:159], v[64:79], v173, v194 op_sel_hi:[0,0,0]
	v_cvt_pk_fp8_f32 v160, v80, v81
	v_cvt_pk_fp8_f32 v161, v84, v85
	v_exp_f32_e32 v88, v88
	v_exp_f32_e32 v89, v89
	v_cvt_pk_fp8_f32 v160, v82, v83 op_sel:[0,0,1]
	v_cvt_pk_fp8_f32 v161, v86, v87 op_sel:[0,0,1]
	v_exp_f32_e32 v90, v90
	v_exp_f32_e32 v91, v91
	v_exp_f32_e32 v92, v92
	v_exp_f32_e32 v93, v93
	v_exp_f32_e32 v94, v94
	v_exp_f32_e32 v95, v95
	s_setprio 0
	ds_read_b128 v[80:83], v224 offset:16384
	ds_read_b128 v[212:215], v224 offset:18432
	ds_read_b128 v[84:87], v225 offset:16384
	ds_read_b128 v[216:219], v225 offset:18432
	v_cvt_pk_fp8_f32 v162, v88, v89
	v_cvt_pk_fp8_f32 v163, v92, v93
	v_exp_f32_e32 v96, v96
	v_exp_f32_e32 v97, v97
	v_cvt_pk_fp8_f32 v162, v90, v91 op_sel:[0,0,1]
	v_cvt_pk_fp8_f32 v163, v94, v95 op_sel:[0,0,1]
	v_exp_f32_e32 v98, v98
	v_exp_f32_e32 v99, v99
	v_exp_f32_e32 v100, v100
	v_exp_f32_e32 v101, v101
	v_exp_f32_e32 v102, v102
	v_exp_f32_e32 v103, v103
	v_mfma_scale_f32_32x32x64_f8f6f4 v[128:143], v[128:135], v[152:159], v[64:79], v173, v194 op_sel_hi:[0,0,0]
	v_cvt_pk_fp8_f32 v164, v96, v97
	v_cvt_pk_fp8_f32 v165, v100, v101
	v_exp_f32_e32 v104, v104
	v_exp_f32_e32 v105, v105
	v_cvt_pk_fp8_f32 v164, v98, v99 op_sel:[0,0,1]
	v_cvt_pk_fp8_f32 v165, v102, v103 op_sel:[0,0,1]
	v_exp_f32_e32 v106, v106
	v_exp_f32_e32 v107, v107
	v_exp_f32_e32 v108, v108
	v_exp_f32_e32 v109, v109
	v_exp_f32_e32 v110, v110
	v_exp_f32_e32 v111, v111
	s_nop 0
	v_cvt_pk_fp8_f32 v166, v104, v105
	v_cvt_pk_fp8_f32 v167, v108, v109
	v_cvt_pk_fp8_f32 v166, v106, v107 op_sel:[0,0,1]
	v_cvt_pk_fp8_f32 v167, v110, v111 op_sel:[0,0,1]
	s_setprio 1
	s_waitcnt lgkmcnt(0)
	v_mfma_scale_f32_32x32x64_f8f6f4 v[32:47], v[80:87], v[160:167], v[32:47], v194, v194 op_sel_hi:[0,0,0]
	v_max3_f32 v88, v112, s5, v113
	v_max3_f32 v88, v88, v114, v115
	v_max3_f32 v88, v88, v116, v117
	v_max3_f32 v88, v88, v118, v119
	v_max3_f32 v88, v88, v120, v121
	v_max3_f32 v88, v88, v122, v123
	v_max3_f32 v88, v88, v124, v125
	v_max3_f32 v88, v88, v126, v127
	s_add_u32 s44, s44, 64
	s_addc_u32 s45, s45, 0
	s_add_u32 m0, s40, 0x8000
	s_nop 0
	global_load_lds_dwordx4 v221, s[44:45]
	v_mfma_scale_f32_32x32x64_f8f6f4 v[16:31], v[212:219], v[160:167], v[16:31], v194, v194 op_sel_hi:[0,0,0]
	v_max3_f32 v80, v128, s5, v129
	v_max3_f32 v80, v80, v130, v131
	v_max3_f32 v80, v80, v132, v133
	v_max3_f32 v80, v80, v134, v135
	v_max3_f32 v80, v80, v136, v137
	v_max3_f32 v80, v80, v138, v139
	v_max3_f32 v80, v80, v140, v141
	v_max3_f32 v80, v80, v142, v143
	s_add_u32 s44, s44, 64
	s_addc_u32 s45, s45, 0
	s_add_u32 m0, s40, 0xa000
	s_nop 0
	global_load_lds_dwordx4 v221, s[44:45]
	v_mfma_scale_f32_32x32x64_f8f6f4 v[48:63], v[144:151], v[160:167], v[48:63], v194, v194 op_sel_hi:[0,0,0]
	s_setprio 0
	v_max_f32_e32 v80, v88, v80
	v_cmp_lt_f32_e32 vcc, s36, v80
	s_cbranch_vccnz .Lat_rare_P15

.Lat_back_P16:
	s_waitcnt vmcnt(0) lgkmcnt(0)
	s_barrier
	ds_read_b128 v[112:115], v222 offset:8192
	ds_read_b128 v[128:131], v222 offset:10240
	ds_read_b128 v[116:119], v223 offset:8192
	ds_read_b128 v[132:135], v223 offset:10240
	s_setprio 1
	v_exp_f32_e32 v80, v80
	v_exp_f32_e32 v81, v81
	v_exp_f32_e32 v82, v82
	v_exp_f32_e32 v83, v83
	v_exp_f32_e32 v84, v84
	v_exp_f32_e32 v85, v85
	v_exp_f32_e32 v86, v86
	v_exp_f32_e32 v87, v87
	s_waitcnt lgkmcnt(0)
	v_mfma_scale_f32_32x32x64_f8f6f4 v[112:127], v[112:119], v[152:159], v[64:79], v173, v194 op_sel_hi:[0,0,0]
	v_cvt_pk_fp8_f32 v160, v80, v81
	v_cvt_pk_fp8_f32 v161, v84, v85
	v_exp_f32_e32 v88, v88
	v_exp_f32_e32 v89, v89
	v_cvt_pk_fp8_f32 v160, v82, v83 op_sel:[0,0,1]
	v_cvt_pk_fp8_f32 v161, v86, v87 op_sel:[0,0,1]
	v_exp_f32_e32 v90, v90
	v_exp_f32_e32 v91, v91
	v_exp_f32_e32 v92, v92
	v_exp_f32_e32 v93, v93
	v_exp_f32_e32 v94, v94
	v_exp_f32_e32 v95, v95
	s_setprio 0
	ds_read_b128 v[80:83], v224 offset:0
	ds_read_b128 v[136:139], v224 offset:2048
	ds_read_b128 v[84:87], v225 offset:0
	ds_read_b128 v[140:143], v225 offset:2048
	v_cvt_pk_fp8_f32 v162, v88, v89
	v_cvt_pk_fp8_f32 v163, v92, v93
	v_exp_f32_e32 v96, v96
	v_exp_f32_e32 v97, v97
	v_cvt_pk_fp8_f32 v162, v90, v91 op_sel:[0,0,1]
	v_cvt_pk_fp8_f32 v163, v94, v95 op_sel:[0,0,1]
	v_exp_f32_e32 v98, v98
	v_exp_f32_e32 v99, v99
	v_exp_f32_e32 v100, v100
	v_exp_f32_e32 v101, v101
	v_exp_f32_e32 v102, v102
	v_exp_f32_e32 v103, v103
	v_mfma_scale_f32_32x32x64_f8f6f4 v[64:79], v[128:135], v[152:159], v[64:79], v173, v194 op_sel_hi:[0,0,0]
	v_cvt_pk_fp8_f32 v164, v96, v97
	v_cvt_pk_fp8_f32 v165, v100, v101
	v_exp_f32_e32 v104, v104
	v_exp_f32_e32 v105, v105
	v_cvt_pk_fp8_f32 v164, v98, v99 op_sel:[0,0,1]
	v_cvt_pk_fp8_f32 v165, v102, v103 op_sel:[0,0,1]
	v_exp_f32_e32 v106, v106
	v_exp_f32_e32 v107, v107
	v_exp_f32_e32 v108, v108
	v_exp_f32_e32 v109, v109
	v_exp_f32_e32 v110, v110
	v_exp_f32_e32 v111, v111
	s_nop 0
	v_cvt_pk_fp8_f32 v166, v104, v105
	v_cvt_pk_fp8_f32 v167, v108, v109
	v_cvt_pk_fp8_f32 v166, v106, v107 op_sel:[0,0,1]
	v_cvt_pk_fp8_f32 v167, v110, v111 op_sel:[0,0,1]
	s_setprio 1
	s_waitcnt lgkmcnt(0)
	v_mfma_scale_f32_32x32x64_f8f6f4 v[32:47], v[80:87], v[160:167], v[32:47], v194, v194 op_sel_hi:[0,0,0]
	v_max3_f32 v88, v112, s5, v113
	v_max3_f32 v88, v88, v114, v115
	v_max3_f32 v88, v88, v116, v117
	v_max3_f32 v88, v88, v118, v119
	v_max3_f32 v88, v88, v120, v121
	v_max3_f32 v88, v88, v122, v123
	v_max3_f32 v88, v88, v124, v125
	v_max3_f32 v88, v88, v126, v127
	v_mfma_scale_f32_32x32x64_f8f6f4 v[16:31], v[136:143], v[160:167], v[16:31], v194, v194 op_sel_hi:[0,0,0]
	v_max3_f32 v80, v64, s5, v65
	v_max3_f32 v80, v80, v66, v67
	v_max3_f32 v80, v80, v68, v69
	v_max3_f32 v80, v80, v70, v71
	v_max3_f32 v80, v80, v72, v73
	v_max3_f32 v80, v80, v74, v75
	v_max3_f32 v80, v80, v76, v77
	v_max3_f32 v80, v80, v78, v79
	v_mfma_scale_f32_32x32x64_f8f6f4 v[48:63], v[144:151], v[160:167], v[48:63], v194, v194 op_sel_hi:[0,0,0]
	s_setprio 0
	v_max_f32_e32 v80, v88, v80
	v_cmp_lt_f32_e32 vcc, s36, v80
	s_cbranch_vccnz .Lat_rare_P17
.LBB3_13:
	ds_read_b128 v[128:131], v224 offset:8192
	ds_read_b128 v[132:135], v225 offset:8192
	ds_read_b128 v[136:139], v224 offset:10240
	ds_read_b128 v[140:143], v225 offset:10240
	s_waitcnt vmcnt(0) lgkmcnt(0)
	s_barrier
	s_andn2_b64 vcc, exec, s[30:31]
	s_cbranch_vccz .LBB3_1
	v_mov_b32_e32 v80, v172
	s_mov_b32 s34, s4
	s_branch .LBB3_2

.Lat_rare_L2:
	v_mov_b32_e32 v113, v112
	s_nop 1
	v_permlane32_swap_b32_e32 v112, v113
	v_max_f32_e32 v112, v112, v113
	v_max_f32_e32 v112, v112, v112
	v_max_f32_e32 v113, 0, v112
	v_exp_f32_e64 v112, -v113
	v_sub_f32_e32 v79, v79, v113
	v_sub_f32_e32 v78, v78, v113
	v_sub_f32_e32 v77, v77, v113
	v_sub_f32_e32 v76, v76, v113
	v_sub_f32_e32 v75, v75, v113
	v_sub_f32_e32 v74, v74, v113
	v_sub_f32_e32 v73, v73, v113
	v_sub_f32_e32 v72, v72, v113
	v_sub_f32_e32 v71, v71, v113
	v_sub_f32_e32 v70, v70, v113
	v_sub_f32_e32 v69, v69, v113
	v_sub_f32_e32 v68, v68, v113
	v_sub_f32_e32 v67, v67, v113
	v_sub_f32_e32 v66, v66, v113
	v_sub_f32_e32 v65, v65, v113
	v_sub_f32_e32 v64, v64, v113
	v_sub_f32_e32 v95, v95, v113
	v_sub_f32_e32 v94, v94, v113
	v_sub_f32_e32 v93, v93, v113
	v_sub_f32_e32 v92, v92, v113
	v_sub_f32_e32 v91, v91, v113
	v_sub_f32_e32 v90, v90, v113
	v_sub_f32_e32 v89, v89, v113
	v_sub_f32_e32 v88, v88, v113
	v_sub_f32_e32 v87, v87, v113
	v_sub_f32_e32 v86, v86, v113
	v_sub_f32_e32 v85, v85, v113
	v_sub_f32_e32 v84, v84, v113
	v_sub_f32_e32 v83, v83, v113
	v_sub_f32_e32 v82, v82, v113
	v_sub_f32_e32 v81, v81, v113
	v_sub_f32_e32 v80, v80, v113
	v_sub_f32_e32 v111, v111, v113
	v_sub_f32_e32 v110, v110, v113
	v_sub_f32_e32 v109, v109, v113
	v_sub_f32_e32 v108, v108, v113
	v_sub_f32_e32 v107, v107, v113
	v_sub_f32_e32 v106, v106, v113
	v_sub_f32_e32 v105, v105, v113
	v_sub_f32_e32 v104, v104, v113
	v_sub_f32_e32 v103, v103, v113
	v_sub_f32_e32 v102, v102, v113
	v_sub_f32_e32 v101, v101, v113
	v_sub_f32_e32 v100, v100, v113
	v_sub_f32_e32 v99, v99, v113
	v_sub_f32_e32 v98, v98, v113
	v_sub_f32_e32 v97, v97, v113
	v_sub_f32_e32 v96, v96, v113
	v_pk_mul_f32 v[46:47], v[112:113], v[46:47] op_sel_hi:[0,1]
	v_pk_mul_f32 v[44:45], v[112:113], v[44:45] op_sel_hi:[0,1]
	v_pk_mul_f32 v[42:43], v[112:113], v[42:43] op_sel_hi:[0,1]
	v_pk_mul_f32 v[40:41], v[112:113], v[40:41] op_sel_hi:[0,1]
	v_pk_mul_f32 v[38:39], v[112:113], v[38:39] op_sel_hi:[0,1]
	v_pk_mul_f32 v[36:37], v[112:113], v[36:37] op_sel_hi:[0,1]
	v_pk_mul_f32 v[34:35], v[112:113], v[34:35] op_sel_hi:[0,1]
	v_pk_mul_f32 v[32:33], v[112:113], v[32:33] op_sel_hi:[0,1]
	v_pk_mul_f32 v[30:31], v[112:113], v[30:31] op_sel_hi:[0,1]
	v_pk_mul_f32 v[28:29], v[112:113], v[28:29] op_sel_hi:[0,1]
	v_pk_mul_f32 v[26:27], v[112:113], v[26:27] op_sel_hi:[0,1]
	v_pk_mul_f32 v[24:25], v[112:113], v[24:25] op_sel_hi:[0,1]
	v_pk_mul_f32 v[22:23], v[112:113], v[22:23] op_sel_hi:[0,1]
	v_pk_mul_f32 v[20:21], v[112:113], v[20:21] op_sel_hi:[0,1]
	v_pk_mul_f32 v[18:19], v[112:113], v[18:19] op_sel_hi:[0,1]
	v_pk_mul_f32 v[16:17], v[112:113], v[16:17] op_sel_hi:[0,1]
	v_pk_mul_f32 v[62:63], v[112:113], v[62:63] op_sel_hi:[0,1]
	v_pk_mul_f32 v[60:61], v[112:113], v[60:61] op_sel_hi:[0,1]
	v_pk_mul_f32 v[58:59], v[112:113], v[58:59] op_sel_hi:[0,1]
	v_pk_mul_f32 v[56:57], v[112:113], v[56:57] op_sel_hi:[0,1]
	v_pk_mul_f32 v[54:55], v[112:113], v[54:55] op_sel_hi:[0,1]
	v_pk_mul_f32 v[52:53], v[112:113], v[52:53] op_sel_hi:[0,1]
	v_pk_mul_f32 v[50:51], v[112:113], v[50:51] op_sel_hi:[0,1]
	v_pk_mul_f32 v[48:49], v[112:113], v[48:49] op_sel_hi:[0,1]
	s_branch .Lat_back_L2
.Lat_rare_L3:
	v_mov_b32_e32 v81, v80
	s_nop 1
	v_permlane32_swap_b32_e32 v80, v81
	v_max_f32_e32 v80, v80, v81
	v_max_f32_e32 v80, v80, v80
	v_max_f32_e32 v81, 0, v80
	v_exp_f32_e64 v80, -v81
	v_sub_f32_e32 v79, v79, v81
	v_sub_f32_e32 v78, v78, v81
	v_sub_f32_e32 v77, v77, v81
	v_sub_f32_e32 v76, v76, v81
	v_sub_f32_e32 v75, v75, v81
	v_sub_f32_e32 v74, v74, v81
	v_sub_f32_e32 v73, v73, v81
	v_sub_f32_e32 v72, v72, v81
	v_sub_f32_e32 v71, v71, v81
	v_sub_f32_e32 v70, v70, v81
	v_sub_f32_e32 v69, v69, v81
	v_sub_f32_e32 v68, v68, v81
	v_sub_f32_e32 v67, v67, v81
	v_sub_f32_e32 v66, v66, v81
	v_sub_f32_e32 v65, v65, v81
	v_sub_f32_e32 v64, v64, v81
	v_sub_f32_e32 v127, v127, v81
	v_sub_f32_e32 v126, v126, v81
	v_sub_f32_e32 v125, v125, v81
	v_sub_f32_e32 v124, v124, v81
	v_sub_f32_e32 v123, v123, v81
	v_sub_f32_e32 v122, v122, v81
	v_sub_f32_e32 v121, v121, v81
	v_sub_f32_e32 v120, v120, v81
	v_sub_f32_e32 v119, v119, v81
	v_sub_f32_e32 v118, v118, v81
	v_sub_f32_e32 v117, v117, v81
	v_sub_f32_e32 v116, v116, v81
	v_sub_f32_e32 v115, v115, v81
	v_sub_f32_e32 v114, v114, v81
	v_sub_f32_e32 v113, v113, v81
	v_sub_f32_e32 v112, v112, v81
	v_sub_f32_e32 v143, v143, v81
	v_sub_f32_e32 v142, v142, v81
	v_sub_f32_e32 v141, v141, v81
	v_sub_f32_e32 v140, v140, v81
	v_sub_f32_e32 v139, v139, v81
	v_sub_f32_e32 v138, v138, v81
	v_sub_f32_e32 v137, v137, v81
	v_sub_f32_e32 v136, v136, v81
	v_sub_f32_e32 v135, v135, v81
	v_sub_f32_e32 v134, v134, v81
	v_sub_f32_e32 v133, v133, v81
	v_sub_f32_e32 v132, v132, v81
	v_sub_f32_e32 v131, v131, v81
	v_sub_f32_e32 v130, v130, v81
	v_sub_f32_e32 v129, v129, v81
	v_sub_f32_e32 v128, v128, v81
	v_pk_mul_f32 v[46:47], v[80:81], v[46:47] op_sel_hi:[0,1]
	v_pk_mul_f32 v[44:45], v[80:81], v[44:45] op_sel_hi:[0,1]
	v_pk_mul_f32 v[42:43], v[80:81], v[42:43] op_sel_hi:[0,1]
	v_pk_mul_f32 v[40:41], v[80:81], v[40:41] op_sel_hi:[0,1]
	v_pk_mul_f32 v[38:39], v[80:81], v[38:39] op_sel_hi:[0,1]
	v_pk_mul_f32 v[36:37], v[80:81], v[36:37] op_sel_hi:[0,1]
	v_pk_mul_f32 v[34:35], v[80:81], v[34:35] op_sel_hi:[0,1]
	v_pk_mul_f32 v[32:33], v[80:81], v[32:33] op_sel_hi:[0,1]
	v_pk_mul_f32 v[30:31], v[80:81], v[30:31] op_sel_hi:[0,1]
	v_pk_mul_f32 v[28:29], v[80:81], v[28:29] op_sel_hi:[0,1]
	v_pk_mul_f32 v[26:27], v[80:81], v[26:27] op_sel_hi:[0,1]
	v_pk_mul_f32 v[24:25], v[80:81], v[24:25] op_sel_hi:[0,1]
	v_pk_mul_f32 v[22:23], v[80:81], v[22:23] op_sel_hi:[0,1]
	v_pk_mul_f32 v[20:21], v[80:81], v[20:21] op_sel_hi:[0,1]
	v_pk_mul_f32 v[18:19], v[80:81], v[18:19] op_sel_hi:[0,1]
	v_pk_mul_f32 v[16:17], v[80:81], v[16:17] op_sel_hi:[0,1]
	v_pk_mul_f32 v[62:63], v[80:81], v[62:63] op_sel_hi:[0,1]
	v_pk_mul_f32 v[60:61], v[80:81], v[60:61] op_sel_hi:[0,1]
	v_pk_mul_f32 v[58:59], v[80:81], v[58:59] op_sel_hi:[0,1]
	v_pk_mul_f32 v[56:57], v[80:81], v[56:57] op_sel_hi:[0,1]
	v_pk_mul_f32 v[54:55], v[80:81], v[54:55] op_sel_hi:[0,1]
	v_pk_mul_f32 v[52:53], v[80:81], v[52:53] op_sel_hi:[0,1]
	v_pk_mul_f32 v[50:51], v[80:81], v[50:51] op_sel_hi:[0,1]
	v_pk_mul_f32 v[48:49], v[80:81], v[48:49] op_sel_hi:[0,1]
	s_branch .Lat_back_L3
.Lat_rare_L4:
	v_mov_b32_e32 v113, v112
	s_nop 1
	v_permlane32_swap_b32_e32 v112, v113
	v_max_f32_e32 v112, v112, v113
	v_max_f32_e32 v112, v112, v112
	v_max_f32_e32 v113, 0, v112
	v_exp_f32_e64 v112, -v113
	v_sub_f32_e32 v79, v79, v113
	v_sub_f32_e32 v78, v78, v113
	v_sub_f32_e32 v77, v77, v113
	v_sub_f32_e32 v76, v76, v113
	v_sub_f32_e32 v75, v75, v113
	v_sub_f32_e32 v74, v74, v113
	v_sub_f32_e32 v73, v73, v113
	v_sub_f32_e32 v72, v72, v113
	v_sub_f32_e32 v71, v71, v113
	v_sub_f32_e32 v70, v70, v113
	v_sub_f32_e32 v69, v69, v113
	v_sub_f32_e32 v68, v68, v113
	v_sub_f32_e32 v67, v67, v113
	v_sub_f32_e32 v66, v66, v113
	v_sub_f32_e32 v65, v65, v113
	v_sub_f32_e32 v64, v64, v113
	v_sub_f32_e32 v95, v95, v113
	v_sub_f32_e32 v94, v94, v113
	v_sub_f32_e32 v93, v93, v113
	v_sub_f32_e32 v92, v92, v113
	v_sub_f32_e32 v91, v91, v113
	v_sub_f32_e32 v90, v90, v113
	v_sub_f32_e32 v89, v89, v113
	v_sub_f32_e32 v88, v88, v113
	v_sub_f32_e32 v87, v87, v113
	v_sub_f32_e32 v86, v86, v113
	v_sub_f32_e32 v85, v85, v113
	v_sub_f32_e32 v84, v84, v113
	v_sub_f32_e32 v83, v83, v113
	v_sub_f32_e32 v82, v82, v113
	v_sub_f32_e32 v81, v81, v113
	v_sub_f32_e32 v80, v80, v113
	v_sub_f32_e32 v111, v111, v113
	v_sub_f32_e32 v110, v110, v113
	v_sub_f32_e32 v109, v109, v113
	v_sub_f32_e32 v108, v108, v113
	v_sub_f32_e32 v107, v107, v113
	v_sub_f32_e32 v106, v106, v113
	v_sub_f32_e32 v105, v105, v113
	v_sub_f32_e32 v104, v104, v113
	v_sub_f32_e32 v103, v103, v113
	v_sub_f32_e32 v102, v102, v113
	v_sub_f32_e32 v101, v101, v113
	v_sub_f32_e32 v100, v100, v113
	v_sub_f32_e32 v99, v99, v113
	v_sub_f32_e32 v98, v98, v113
	v_sub_f32_e32 v97, v97, v113
	v_sub_f32_e32 v96, v96, v113
	v_pk_mul_f32 v[46:47], v[112:113], v[46:47] op_sel_hi:[0,1]
	v_pk_mul_f32 v[44:45], v[112:113], v[44:45] op_sel_hi:[0,1]
	v_pk_mul_f32 v[42:43], v[112:113], v[42:43] op_sel_hi:[0,1]
	v_pk_mul_f32 v[40:41], v[112:113], v[40:41] op_sel_hi:[0,1]
	v_pk_mul_f32 v[38:39], v[112:113], v[38:39] op_sel_hi:[0,1]
	v_pk_mul_f32 v[36:37], v[112:113], v[36:37] op_sel_hi:[0,1]
	v_pk_mul_f32 v[34:35], v[112:113], v[34:35] op_sel_hi:[0,1]
	v_pk_mul_f32 v[32:33], v[112:113], v[32:33] op_sel_hi:[0,1]
	v_pk_mul_f32 v[30:31], v[112:113], v[30:31] op_sel_hi:[0,1]
	v_pk_mul_f32 v[28:29], v[112:113], v[28:29] op_sel_hi:[0,1]
	v_pk_mul_f32 v[26:27], v[112:113], v[26:27] op_sel_hi:[0,1]
	v_pk_mul_f32 v[24:25], v[112:113], v[24:25] op_sel_hi:[0,1]
	v_pk_mul_f32 v[22:23], v[112:113], v[22:23] op_sel_hi:[0,1]
	v_pk_mul_f32 v[20:21], v[112:113], v[20:21] op_sel_hi:[0,1]
	v_pk_mul_f32 v[18:19], v[112:113], v[18:19] op_sel_hi:[0,1]
	v_pk_mul_f32 v[16:17], v[112:113], v[16:17] op_sel_hi:[0,1]
	v_pk_mul_f32 v[62:63], v[112:113], v[62:63] op_sel_hi:[0,1]
	v_pk_mul_f32 v[60:61], v[112:113], v[60:61] op_sel_hi:[0,1]
	v_pk_mul_f32 v[58:59], v[112:113], v[58:59] op_sel_hi:[0,1]
	v_pk_mul_f32 v[56:57], v[112:113], v[56:57] op_sel_hi:[0,1]
	v_pk_mul_f32 v[54:55], v[112:113], v[54:55] op_sel_hi:[0,1]
	v_pk_mul_f32 v[52:53], v[112:113], v[52:53] op_sel_hi:[0,1]
	v_pk_mul_f32 v[50:51], v[112:113], v[50:51] op_sel_hi:[0,1]
	v_pk_mul_f32 v[48:49], v[112:113], v[48:49] op_sel_hi:[0,1]
	s_branch .Lat_back_L4
.Lat_rare_P13:
	v_mov_b32_e32 v81, v80
	s_nop 1
	v_permlane32_swap_b32_e32 v80, v81
	v_max_f32_e32 v80, v80, v81
	v_max_f32_e32 v80, v80, v80
	v_max_f32_e32 v81, 0, v80
	v_exp_f32_e64 v80, -v81
	v_sub_f32_e32 v79, v79, v81
	v_sub_f32_e32 v78, v78, v81
	v_sub_f32_e32 v77, v77, v81
	v_sub_f32_e32 v76, v76, v81
	v_sub_f32_e32 v75, v75, v81
	v_sub_f32_e32 v74, v74, v81
	v_sub_f32_e32 v73, v73, v81
	v_sub_f32_e32 v72, v72, v81
	v_sub_f32_e32 v71, v71, v81
	v_sub_f32_e32 v70, v70, v81
	v_sub_f32_e32 v69, v69, v81
	v_sub_f32_e32 v68, v68, v81
	v_sub_f32_e32 v67, v67, v81
	v_sub_f32_e32 v66, v66, v81
	v_sub_f32_e32 v65, v65, v81
	v_sub_f32_e32 v64, v64, v81
	v_sub_f32_e32 v127, v127, v81
	v_sub_f32_e32 v126, v126, v81
	v_sub_f32_e32 v125, v125, v81
	v_sub_f32_e32 v124, v124, v81
	v_sub_f32_e32 v123, v123, v81
	v_sub_f32_e32 v122, v122, v81
	v_sub_f32_e32 v121, v121, v81
	v_sub_f32_e32 v120, v120, v81
	v_sub_f32_e32 v119, v119, v81
	v_sub_f32_e32 v118, v118, v81
	v_sub_f32_e32 v117, v117, v81
	v_sub_f32_e32 v116, v116, v81
	v_sub_f32_e32 v115, v115, v81
	v_sub_f32_e32 v114, v114, v81
	v_sub_f32_e32 v113, v113, v81
	v_sub_f32_e32 v112, v112, v81
	v_sub_f32_e32 v143, v143, v81
	v_sub_f32_e32 v142, v142, v81
	v_sub_f32_e32 v141, v141, v81
	v_sub_f32_e32 v140, v140, v81
	v_sub_f32_e32 v139, v139, v81
	v_sub_f32_e32 v138, v138, v81
	v_sub_f32_e32 v137, v137, v81
	v_sub_f32_e32 v136, v136, v81
	v_sub_f32_e32 v135, v135, v81
	v_sub_f32_e32 v134, v134, v81
	v_sub_f32_e32 v133, v133, v81
	v_sub_f32_e32 v132, v132, v81
	v_sub_f32_e32 v131, v131, v81
	v_sub_f32_e32 v130, v130, v81
	v_sub_f32_e32 v129, v129, v81
	v_sub_f32_e32 v128, v128, v81
	v_pk_mul_f32 v[46:47], v[80:81], v[46:47] op_sel_hi:[0,1]
	v_pk_mul_f32 v[44:45], v[80:81], v[44:45] op_sel_hi:[0,1]
	v_pk_mul_f32 v[42:43], v[80:81], v[42:43] op_sel_hi:[0,1]
	v_pk_mul_f32 v[40:41], v[80:81], v[40:41] op_sel_hi:[0,1]
	v_pk_mul_f32 v[38:39], v[80:81], v[38:39] op_sel_hi:[0,1]
	v_pk_mul_f32 v[36:37], v[80:81], v[36:37] op_sel_hi:[0,1]
	v_pk_mul_f32 v[34:35], v[80:81], v[34:35] op_sel_hi:[0,1]
	v_pk_mul_f32 v[32:33], v[80:81], v[32:33] op_sel_hi:[0,1]
	v_pk_mul_f32 v[30:31], v[80:81], v[30:31] op_sel_hi:[0,1]
	v_pk_mul_f32 v[28:29], v[80:81], v[28:29] op_sel_hi:[0,1]
	v_pk_mul_f32 v[26:27], v[80:81], v[26:27] op_sel_hi:[0,1]
	v_pk_mul_f32 v[24:25], v[80:81], v[24:25] op_sel_hi:[0,1]
	v_pk_mul_f32 v[22:23], v[80:81], v[22:23] op_sel_hi:[0,1]
	v_pk_mul_f32 v[20:21], v[80:81], v[20:21] op_sel_hi:[0,1]
	v_pk_mul_f32 v[18:19], v[80:81], v[18:19] op_sel_hi:[0,1]
	v_pk_mul_f32 v[16:17], v[80:81], v[16:17] op_sel_hi:[0,1]
	v_pk_mul_f32 v[62:63], v[80:81], v[62:63] op_sel_hi:[0,1]
	v_pk_mul_f32 v[60:61], v[80:81], v[60:61] op_sel_hi:[0,1]
	v_pk_mul_f32 v[58:59], v[80:81], v[58:59] op_sel_hi:[0,1]
	v_pk_mul_f32 v[56:57], v[80:81], v[56:57] op_sel_hi:[0,1]
	v_pk_mul_f32 v[54:55], v[80:81], v[54:55] op_sel_hi:[0,1]
	v_pk_mul_f32 v[52:53], v[80:81], v[52:53] op_sel_hi:[0,1]
	v_pk_mul_f32 v[50:51], v[80:81], v[50:51] op_sel_hi:[0,1]
	v_pk_mul_f32 v[48:49], v[80:81], v[48:49] op_sel_hi:[0,1]
	s_branch .Lat_back_P13
.Lat_rare_P14:
	v_mov_b32_e32 v113, v112
	s_nop 1
	v_permlane32_swap_b32_e32 v112, v113
	v_max_f32_e32 v112, v112, v113
	v_max_f32_e32 v112, v112, v112
	v_max_f32_e32 v113, 0, v112
	v_exp_f32_e64 v112, -v113
	v_sub_f32_e32 v79, v79, v113
	v_sub_f32_e32 v78, v78, v113
	v_sub_f32_e32 v77, v77, v113
	v_sub_f32_e32 v76, v76, v113
	v_sub_f32_e32 v75, v75, v113
	v_sub_f32_e32 v74, v74, v113
	v_sub_f32_e32 v73, v73, v113
	v_sub_f32_e32 v72, v72, v113
	v_sub_f32_e32 v71, v71, v113
	v_sub_f32_e32 v70, v70, v113
	v_sub_f32_e32 v69, v69, v113
	v_sub_f32_e32 v68, v68, v113
	v_sub_f32_e32 v67, v67, v113
	v_sub_f32_e32 v66, v66, v113
	v_sub_f32_e32 v65, v65, v113
	v_sub_f32_e32 v64, v64, v113
	v_sub_f32_e32 v95, v95, v113
	v_sub_f32_e32 v94, v94, v113
	v_sub_f32_e32 v93, v93, v113
	v_sub_f32_e32 v92, v92, v113
	v_sub_f32_e32 v91, v91, v113
	v_sub_f32_e32 v90, v90, v113
	v_sub_f32_e32 v89, v89, v113
	v_sub_f32_e32 v88, v88, v113
	v_sub_f32_e32 v87, v87, v113
	v_sub_f32_e32 v86, v86, v113
	v_sub_f32_e32 v85, v85, v113
	v_sub_f32_e32 v84, v84, v113
	v_sub_f32_e32 v83, v83, v113
	v_sub_f32_e32 v82, v82, v113
	v_sub_f32_e32 v81, v81, v113
	v_sub_f32_e32 v80, v80, v113
	v_sub_f32_e32 v111, v111, v113
	v_sub_f32_e32 v110, v110, v113
	v_sub_f32_e32 v109, v109, v113
	v_sub_f32_e32 v108, v108, v113
	v_sub_f32_e32 v107, v107, v113
	v_sub_f32_e32 v106, v106, v113
	v_sub_f32_e32 v105, v105, v113
	v_sub_f32_e32 v104, v104, v113
	v_sub_f32_e32 v103, v103, v113
	v_sub_f32_e32 v102, v102, v113
	v_sub_f32_e32 v101, v101, v113
	v_sub_f32_e32 v100, v100, v113
	v_sub_f32_e32 v99, v99, v113
	v_sub_f32_e32 v98, v98, v113
	v_sub_f32_e32 v97, v97, v113
	v_sub_f32_e32 v96, v96, v113
	v_pk_mul_f32 v[46:47], v[112:113], v[46:47] op_sel_hi:[0,1]
	v_pk_mul_f32 v[44:45], v[112:113], v[44:45] op_sel_hi:[0,1]
	v_pk_mul_f32 v[42:43], v[112:113], v[42:43] op_sel_hi:[0,1]
	v_pk_mul_f32 v[40:41], v[112:113], v[40:41] op_sel_hi:[0,1]
	v_pk_mul_f32 v[38:39], v[112:113], v[38:39] op_sel_hi:[0,1]
	v_pk_mul_f32 v[36:37], v[112:113], v[36:37] op_sel_hi:[0,1]
	v_pk_mul_f32 v[34:35], v[112:113], v[34:35] op_sel_hi:[0,1]
	v_pk_mul_f32 v[32:33], v[112:113], v[32:33] op_sel_hi:[0,1]
	v_pk_mul_f32 v[30:31], v[112:113], v[30:31] op_sel_hi:[0,1]
	v_pk_mul_f32 v[28:29], v[112:113], v[28:29] op_sel_hi:[0,1]
	v_pk_mul_f32 v[26:27], v[112:113], v[26:27] op_sel_hi:[0,1]
	v_pk_mul_f32 v[24:25], v[112:113], v[24:25] op_sel_hi:[0,1]
	v_pk_mul_f32 v[22:23], v[112:113], v[22:23] op_sel_hi:[0,1]
	v_pk_mul_f32 v[20:21], v[112:113], v[20:21] op_sel_hi:[0,1]
	v_pk_mul_f32 v[18:19], v[112:113], v[18:19] op_sel_hi:[0,1]
	v_pk_mul_f32 v[16:17], v[112:113], v[16:17] op_sel_hi:[0,1]
	v_pk_mul_f32 v[62:63], v[112:113], v[62:63] op_sel_hi:[0,1]
	v_pk_mul_f32 v[60:61], v[112:113], v[60:61] op_sel_hi:[0,1]
	v_pk_mul_f32 v[58:59], v[112:113], v[58:59] op_sel_hi:[0,1]
	v_pk_mul_f32 v[56:57], v[112:113], v[56:57] op_sel_hi:[0,1]
	v_pk_mul_f32 v[54:55], v[112:113], v[54:55] op_sel_hi:[0,1]
	v_pk_mul_f32 v[52:53], v[112:113], v[52:53] op_sel_hi:[0,1]
	v_pk_mul_f32 v[50:51], v[112:113], v[50:51] op_sel_hi:[0,1]
	v_pk_mul_f32 v[48:49], v[112:113], v[48:49] op_sel_hi:[0,1]
	s_branch .Lat_back_P14
.Lat_rare_P15:
	v_mov_b32_e32 v81, v80
	s_nop 1
	v_permlane32_swap_b32_e32 v80, v81
	v_max_f32_e32 v80, v80, v81
	v_max_f32_e32 v80, v80, v80
	v_max_f32_e32 v81, 0, v80
	v_exp_f32_e64 v80, -v81
	v_sub_f32_e32 v79, v79, v81
	v_sub_f32_e32 v78, v78, v81
	v_sub_f32_e32 v77, v77, v81
	v_sub_f32_e32 v76, v76, v81
	v_sub_f32_e32 v75, v75, v81
	v_sub_f32_e32 v74, v74, v81
	v_sub_f32_e32 v73, v73, v81
	v_sub_f32_e32 v72, v72, v81
	v_sub_f32_e32 v71, v71, v81
	v_sub_f32_e32 v70, v70, v81
	v_sub_f32_e32 v69, v69, v81
	v_sub_f32_e32 v68, v68, v81
	v_sub_f32_e32 v67, v67, v81
	v_sub_f32_e32 v66, v66, v81
	v_sub_f32_e32 v65, v65, v81
	v_sub_f32_e32 v64, v64, v81
	v_sub_f32_e32 v127, v127, v81
	v_sub_f32_e32 v126, v126, v81
	v_sub_f32_e32 v125, v125, v81
	v_sub_f32_e32 v124, v124, v81
	v_sub_f32_e32 v123, v123, v81
	v_sub_f32_e32 v122, v122, v81
	v_sub_f32_e32 v121, v121, v81
	v_sub_f32_e32 v120, v120, v81
	v_sub_f32_e32 v119, v119, v81
	v_sub_f32_e32 v118, v118, v81
	v_sub_f32_e32 v117, v117, v81
	v_sub_f32_e32 v116, v116, v81
	v_sub_f32_e32 v115, v115, v81
	v_sub_f32_e32 v114, v114, v81
	v_sub_f32_e32 v113, v113, v81
	v_sub_f32_e32 v112, v112, v81
	v_sub_f32_e32 v143, v143, v81
	v_sub_f32_e32 v142, v142, v81
	v_sub_f32_e32 v141, v141, v81
	v_sub_f32_e32 v140, v140, v81
	v_sub_f32_e32 v139, v139, v81
	v_sub_f32_e32 v138, v138, v81
	v_sub_f32_e32 v137, v137, v81
	v_sub_f32_e32 v136, v136, v81
	v_sub_f32_e32 v135, v135, v81
	v_sub_f32_e32 v134, v134, v81
	v_sub_f32_e32 v133, v133, v81
	v_sub_f32_e32 v132, v132, v81
	v_sub_f32_e32 v131, v131, v81
	v_sub_f32_e32 v130, v130, v81
	v_sub_f32_e32 v129, v129, v81
	v_sub_f32_e32 v128, v128, v81
	v_pk_mul_f32 v[46:47], v[80:81], v[46:47] op_sel_hi:[0,1]
	v_pk_mul_f32 v[44:45], v[80:81], v[44:45] op_sel_hi:[0,1]
	v_pk_mul_f32 v[42:43], v[80:81], v[42:43] op_sel_hi:[0,1]
	v_pk_mul_f32 v[40:41], v[80:81], v[40:41] op_sel_hi:[0,1]
	v_pk_mul_f32 v[38:39], v[80:81], v[38:39] op_sel_hi:[0,1]
	v_pk_mul_f32 v[36:37], v[80:81], v[36:37] op_sel_hi:[0,1]
	v_pk_mul_f32 v[34:35], v[80:81], v[34:35] op_sel_hi:[0,1]
	v_pk_mul_f32 v[32:33], v[80:81], v[32:33] op_sel_hi:[0,1]
	v_pk_mul_f32 v[30:31], v[80:81], v[30:31] op_sel_hi:[0,1]
	v_pk_mul_f32 v[28:29], v[80:81], v[28:29] op_sel_hi:[0,1]
	v_pk_mul_f32 v[26:27], v[80:81], v[26:27] op_sel_hi:[0,1]
	v_pk_mul_f32 v[24:25], v[80:81], v[24:25] op_sel_hi:[0,1]
	v_pk_mul_f32 v[22:23], v[80:81], v[22:23] op_sel_hi:[0,1]
	v_pk_mul_f32 v[20:21], v[80:81], v[20:21] op_sel_hi:[0,1]
	v_pk_mul_f32 v[18:19], v[80:81], v[18:19] op_sel_hi:[0,1]
	v_pk_mul_f32 v[16:17], v[80:81], v[16:17] op_sel_hi:[0,1]
	v_pk_mul_f32 v[62:63], v[80:81], v[62:63] op_sel_hi:[0,1]
	v_pk_mul_f32 v[60:61], v[80:81], v[60:61] op_sel_hi:[0,1]
	v_pk_mul_f32 v[58:59], v[80:81], v[58:59] op_sel_hi:[0,1]
	v_pk_mul_f32 v[56:57], v[80:81], v[56:57] op_sel_hi:[0,1]
	v_pk_mul_f32 v[54:55], v[80:81], v[54:55] op_sel_hi:[0,1]
	v_pk_mul_f32 v[52:53], v[80:81], v[52:53] op_sel_hi:[0,1]
	v_pk_mul_f32 v[50:51], v[80:81], v[50:51] op_sel_hi:[0,1]
	v_pk_mul_f32 v[48:49], v[80:81], v[48:49] op_sel_hi:[0,1]
	s_branch .Lat_back_P15

	.amdhsa_kernel _Z13attn11_kernelILi4EEvPc
		.amdhsa_group_segment_fixed_size 16384
		.amdhsa_private_segment_fixed_size 0
		.amdhsa_kernarg_size 264
		.amdhsa_user_sgpr_count 2
		.amdhsa_user_sgpr_dispatch_ptr 0
		.amdhsa_user_sgpr_queue_ptr 0
		.amdhsa_user_sgpr_kernarg_segment_ptr 1
		.amdhsa_user_sgpr_dispatch_id 0
		.amdhsa_user_sgpr_kernarg_preload_length 0
		.amdhsa_user_sgpr_kernarg_preload_offset 0
		.amdhsa_user_sgpr_private_segment_size 0
		.amdhsa_uses_dynamic_stack 0
		.amdhsa_enable_private_segment 0
		.amdhsa_system_sgpr_workgroup_id_x 1
		.amdhsa_system_sgpr_workgroup_id_y 0
		.amdhsa_system_sgpr_workgroup_id_z 0
		.amdhsa_system_sgpr_workgroup_info 0
		.amdhsa_system_vgpr_workitem_id 0
		.amdhsa_next_free_vgpr 226
		.amdhsa_next_free_sgpr 56
		.amdhsa_accum_offset 228
		.amdhsa_reserve_vcc 1
		.amdhsa_float_round_mode_32 0
		.amdhsa_float_round_mode_16_64 0
		.amdhsa_float_denorm_mode_32 3
		.amdhsa_float_denorm_mode_16_64 3
		.amdhsa_dx10_clamp 1
		.amdhsa_ieee_mode 1
		.amdhsa_fp16_overflow 0
		.amdhsa_tg_split 0
		.amdhsa_exception_fp_ieee_invalid_op 0
		.amdhsa_exception_fp_denorm_src 0
		.amdhsa_exception_fp_ieee_div_zero 0
		.amdhsa_exception_fp_ieee_overflow 0
		.amdhsa_exception_fp_ieee_underflow 0
		.amdhsa_exception_fp_ieee_inexact 0
		.amdhsa_exception_int_div_zero 0
	.end_amdhsa_kernel

amdhsa.kernels:
  - .agpr_count:     0
    .args:
      - .actual_access:  read_only
        .address_space:  global
        .offset:         0
        .size:           8
        .value_kind:     global_buffer
      - .actual_access:  read_only
        .address_space:  global
        .offset:         8
        .size:           8
        .value_kind:     global_buffer
      - .actual_access:  read_only
        .address_space:  global
        .offset:         16
        .size:           8
        .value_kind:     global_buffer
      - .actual_access:  read_only
        .address_space:  global
        .offset:         24
        .size:           8
        .value_kind:     global_buffer
      - .actual_access:  read_only
        .address_space:  global
        .offset:         32
        .size:           8
        .value_kind:     global_buffer
      - .actual_access:  read_only
        .address_space:  global
        .offset:         40
        .size:           8
        .value_kind:     global_buffer
      - .actual_access:  read_only
        .address_space:  global
        .offset:         48
        .size:           8
        .value_kind:     global_buffer
      - .actual_access:  write_only
        .address_space:  global
        .offset:         56
        .size:           8
        .value_kind:     global_buffer
    .group_segment_fixed_size: 32
    .kernarg_segment_align: 8
    .kernarg_segment_size: 64
    .language:       OpenCL C
    .language_version:
      - 2
      - 0
    .max_flat_workgroup_size: 256
    .name:           _Z11prep_kernelPKfS0_S0_S0_S0_S0_S0_Pc
    .private_segment_fixed_size: 0
    .sgpr_count:     48
    .sgpr_spill_count: 0
    .symbol:         _Z11prep_kernelPKfS0_S0_S0_S0_S0_S0_Pc.kd
    .uniform_work_group_size: 1
    .uses_dynamic_stack: false
    .vgpr_count:     78
    .vgpr_spill_count: 0
    .wavefront_size: 64
  - .agpr_count:     0
    .args:
      - .address_space:  global
        .offset:         0
        .size:           8
        .value_kind:     global_buffer
      - .actual_access:  read_only
        .address_space:  global
        .offset:         8
        .size:           8
        .value_kind:     global_buffer
      - .actual_access:  read_only
        .address_space:  global
        .offset:         16
        .size:           8
        .value_kind:     global_buffer
    .group_segment_fixed_size: 0
    .kernarg_segment_align: 8
    .kernarg_segment_size: 24
    .language:       OpenCL C
    .language_version:
      - 2
      - 0
    .max_flat_workgroup_size: 512
    .name:           _Z13qkv256_kernelPcPKfS1_
    .private_segment_fixed_size: 0
    .sgpr_count:     35
    .sgpr_spill_count: 0
    .symbol:         _Z13qkv256_kernelPcPKfS1_.kd
    .uniform_work_group_size: 1
    .uses_dynamic_stack: false
    .vgpr_count:     214
    .vgpr_spill_count: 0
    .wavefront_size: 64
  - .agpr_count:     0
    .args:
      - .address_space:  global
        .offset:         0
        .size:           8
        .value_kind:     global_buffer
      - .actual_access:  read_only
        .address_space:  global
        .offset:         8
        .size:           8
        .value_kind:     global_buffer
      - .actual_access:  read_only
        .address_space:  global
        .offset:         16
        .size:           8
        .value_kind:     global_buffer
      - .actual_access:  write_only
        .address_space:  global
        .offset:         24
        .size:           8
        .value_kind:     global_buffer
    .group_segment_fixed_size: 0
    .kernarg_segment_align: 8
    .kernarg_segment_size: 32
    .language:       OpenCL C
    .language_version:
      - 2
      - 0
    .max_flat_workgroup_size: 256
    .name:           _Z11proj_kernelPKcPKfS2_Pf
    .private_segment_fixed_size: 0
    .sgpr_count:     34
    .sgpr_spill_count: 0
    .symbol:         _Z11proj_kernelPKcPKfS2_Pf.kd
    .uniform_work_group_size: 1
    .uses_dynamic_stack: false
    .vgpr_count:     185
    .vgpr_spill_count: 0
    .wavefront_size: 64
  - .agpr_count:     0
    .args:
      - .address_space:  global
        .offset:         0
        .size:           8
        .value_kind:     global_buffer
      - .offset:         8
        .size:           4
        .value_kind:     hidden_block_count_x
      - .offset:         12
        .size:           4
        .value_kind:     hidden_block_count_y
      - .offset:         16
        .size:           4
        .value_kind:     hidden_block_count_z
      - .offset:         20
        .size:           2
        .value_kind:     hidden_group_size_x
      - .offset:         22
        .size:           2
        .value_kind:     hidden_group_size_y
      - .offset:         24
        .size:           2
        .value_kind:     hidden_group_size_z
      - .offset:         26
        .size:           2
        .value_kind:     hidden_remainder_x
      - .offset:         28
        .size:           2
        .value_kind:     hidden_remainder_y
      - .offset:         30
        .size:           2
        .value_kind:     hidden_remainder_z
      - .offset:         48
        .size:           8
        .value_kind:     hidden_global_offset_x
      - .offset:         56
        .size:           8
        .value_kind:     hidden_global_offset_y
      - .offset:         64
        .size:           8
        .value_kind:     hidden_global_offset_z
      - .offset:         72
        .size:           2
        .value_kind:     hidden_grid_dims
      - .offset:         128
        .size:           4
        .value_kind:     hidden_dynamic_lds_size
    .group_segment_fixed_size: 16384
    .kernarg_segment_align: 8
    .kernarg_segment_size: 264
    .language:       OpenCL C
    .language_version:
      - 2
      - 0
    .max_flat_workgroup_size: 256
    .name:           _Z13attn11_kernelILi4EEvPc
    .private_segment_fixed_size: 0
    .sgpr_count:     62
    .sgpr_spill_count: 0
    .symbol:         _Z13attn11_kernelILi4EEvPc.kd
    .uniform_work_group_size: 1
    .uses_dynamic_stack: false
    .vgpr_count:     226
    .vgpr_spill_count: 0
    .wavefront_size: 64
